# baseline (speedup 1.0000x reference)
.LBB6_12:
	ds_read_b128 v[176:179], v169
	ds_read_b128 v[184:187], v171
	ds_read_b128 v[180:183], v170
	ds_read_b128 v[188:191], v172
	v_add_u32_e32 v174, 0xc000, v152
	v_lshl_add_u64 v[192:193], v[136:137], 0, s[44:45]
	v_add_u32_e32 v175, 0xe000, v152
	v_add_u32_e32 v173, s17, v168
	v_lshl_add_u64 v[232:233], v[192:193], 0, s[30:31]
	s_mov_b32 m0, s72
	v_lshl_add_u64 v[248:249], v[134:135], 0, s[44:45]
	ds_read_b128 v[196:199], v173
	ds_read_b128 v[204:207], v173 offset:2048
	ds_read_b128 v[216:219], v173 offset:4096
	ds_read_b128 v[224:227], v173 offset:6144
	ds_read_b128 v[200:203], v173 offset:1024
	ds_read_b128 v[212:215], v173 offset:3072
	ds_read_b128 v[220:223], v173 offset:5120
	ds_read_b128 v[228:231], v173 offset:7168
	global_load_lds_dwordx4 v[232:233], off
	s_mov_b32 m0, s73
	v_lshl_add_u64 v[232:233], v[248:249], 0, s[30:31]
	global_load_lds_dwordx4 v[232:233], off
	s_waitcnt lgkmcnt(8)
	s_barrier
	s_waitcnt lgkmcnt(4)
	v_mfma_f32_16x16x32_f16 v[2:5], v[196:199], v[176:179], v[2:5]
	v_mfma_f32_16x16x32_f16 v[6:9], v[196:199], v[184:187], v[6:9]
	v_mfma_f32_16x16x32_f16 v[10:13], v[204:207], v[176:179], v[10:13]
	v_mfma_f32_16x16x32_f16 v[18:21], v[204:207], v[184:187], v[18:21]
	v_mfma_f32_16x16x32_f16 v[30:33], v[216:219], v[176:179], v[30:33]
	v_mfma_f32_16x16x32_f16 v[42:45], v[216:219], v[184:187], v[42:45]
	v_mfma_f32_16x16x32_f16 v[54:57], v[224:227], v[176:179], v[54:57]
	v_mfma_f32_16x16x32_f16 v[66:69], v[224:227], v[184:187], v[66:69]
	s_waitcnt lgkmcnt(0)
	v_mfma_f32_16x16x32_f16 v[2:5], v[200:203], v[180:183], v[2:5]
	v_mfma_f32_16x16x32_f16 v[6:9], v[200:203], v[188:191], v[6:9]
	v_mfma_f32_16x16x32_f16 v[10:13], v[212:215], v[180:183], v[10:13]
	v_mfma_f32_16x16x32_f16 v[18:21], v[212:215], v[188:191], v[18:21]
	v_mfma_f32_16x16x32_f16 v[30:33], v[220:223], v[180:183], v[30:33]
	v_mfma_f32_16x16x32_f16 v[42:45], v[220:223], v[188:191], v[42:45]
	v_mfma_f32_16x16x32_f16 v[54:57], v[228:231], v[180:183], v[54:57]
	v_mfma_f32_16x16x32_f16 v[66:69], v[228:231], v[188:191], v[66:69]
	s_barrier
	v_lshl_add_u64 v[250:251], v[140:141], 0, s[44:45]
	v_lshl_add_u64 v[252:253], v[250:251], 0, s[34:35]
	s_mov_b32 m0, s74
	ds_read_b128 v[232:235], v161
	ds_read_b128 v[240:243], v163
	ds_read_b128 v[236:239], v162
	ds_read_b128 v[244:247], v164
	global_load_lds_dwordx4 v[252:253], off
	v_lshl_add_u64 v[252:253], v[138:139], 0, s[44:45]
	s_mov_b32 m0, s75
	v_lshl_add_u64 v[254:255], v[252:253], 0, s[34:35]
	global_load_lds_dwordx4 v[254:255], off
	s_barrier
	s_waitcnt lgkmcnt(2)
	v_mfma_f32_16x16x32_f16 v[14:17], v[196:199], v[232:235], v[14:17]
	v_mfma_f32_16x16x32_f16 v[22:25], v[196:199], v[240:243], v[22:25]
	v_mfma_f32_16x16x32_f16 v[34:37], v[204:207], v[232:235], v[34:37]
	v_mfma_f32_16x16x32_f16 v[46:49], v[204:207], v[240:243], v[46:49]
	v_mfma_f32_16x16x32_f16 v[58:61], v[216:219], v[232:235], v[58:61]
	v_mfma_f32_16x16x32_f16 v[70:73], v[216:219], v[240:243], v[70:73]
	v_mfma_f32_16x16x32_f16 v[78:81], v[224:227], v[232:235], v[78:81]
	v_mfma_f32_16x16x32_f16 v[86:89], v[224:227], v[240:243], v[86:89]
	s_waitcnt lgkmcnt(0)
	v_mfma_f32_16x16x32_f16 v[14:17], v[200:203], v[236:239], v[14:17]
	v_mfma_f32_16x16x32_f16 v[22:25], v[200:203], v[244:247], v[22:25]
	v_mfma_f32_16x16x32_f16 v[34:37], v[212:215], v[236:239], v[34:37]
	v_mfma_f32_16x16x32_f16 v[46:49], v[212:215], v[244:247], v[46:49]
	v_mfma_f32_16x16x32_f16 v[58:61], v[220:223], v[236:239], v[58:61]
	v_mfma_f32_16x16x32_f16 v[70:73], v[220:223], v[244:247], v[70:73]
	v_mfma_f32_16x16x32_f16 v[78:81], v[228:231], v[236:239], v[78:81]
	v_mfma_f32_16x16x32_f16 v[86:89], v[228:231], v[244:247], v[86:89]
	v_lshl_add_u64 v[254:255], v[192:193], 0, s[34:35]
	s_mov_b32 m0, s76
	s_barrier
	ds_read_b128 v[196:199], v173 offset:16384
	ds_read_b128 v[204:207], v173 offset:18432
	ds_read_b128 v[216:219], v173 offset:20480
	ds_read_b128 v[224:227], v173 offset:22528
	ds_read_b128 v[200:203], v173 offset:17408
	ds_read_b128 v[212:215], v173 offset:19456
	ds_read_b128 v[220:223], v173 offset:21504
	ds_read_b128 v[228:231], v173 offset:23552
	global_load_lds_dwordx4 v[254:255], off
	s_mov_b32 m0, s77
	v_lshl_add_u64 v[254:255], v[248:249], 0, s[34:35]
	global_load_lds_dwordx4 v[254:255], off
	s_barrier
	s_waitcnt lgkmcnt(4)
	v_mfma_f32_16x16x32_f16 v[26:29], v[196:199], v[176:179], v[26:29]
	v_mfma_f32_16x16x32_f16 v[38:41], v[196:199], v[184:187], v[38:41]
	v_mfma_f32_16x16x32_f16 v[50:53], v[204:207], v[176:179], v[50:53]
	v_mfma_f32_16x16x32_f16 v[62:65], v[204:207], v[184:187], v[62:65]
	v_mfma_f32_16x16x32_f16 v[74:77], v[216:219], v[176:179], v[74:77]
	v_mfma_f32_16x16x32_f16 v[82:85], v[216:219], v[184:187], v[82:85]
	v_mfma_f32_16x16x32_f16 v[90:93], v[224:227], v[176:179], v[90:93]
	v_mfma_f32_16x16x32_f16 v[94:97], v[224:227], v[184:187], v[94:97]
	s_waitcnt lgkmcnt(0)
	v_mfma_f32_16x16x32_f16 v[26:29], v[200:203], v[180:183], v[26:29]
	v_mfma_f32_16x16x32_f16 v[38:41], v[200:203], v[188:191], v[38:41]
	v_mfma_f32_16x16x32_f16 v[50:53], v[212:215], v[180:183], v[50:53]
	v_mfma_f32_16x16x32_f16 v[62:65], v[212:215], v[188:191], v[62:65]
	v_mfma_f32_16x16x32_f16 v[74:77], v[220:223], v[180:183], v[74:77]
	v_mfma_f32_16x16x32_f16 v[82:85], v[220:223], v[188:191], v[82:85]
	v_mfma_f32_16x16x32_f16 v[90:93], v[228:231], v[180:183], v[90:93]
	v_mfma_f32_16x16x32_f16 v[94:97], v[228:231], v[188:191], v[94:97]
	s_barrier
	s_mov_b32 m0, s78
	v_lshl_add_u64 v[176:177], v[250:251], 0, s[36:37]
	global_load_lds_dwordx4 v[176:177], off
	s_mov_b32 m0, s79
	v_lshl_add_u64 v[176:177], v[252:253], 0, s[36:37]
	global_load_lds_dwordx4 v[176:177], off
	s_waitcnt vmcnt(6)
	s_barrier
	v_mfma_f32_16x16x32_f16 v[98:101], v[196:199], v[232:235], v[98:101]
	v_mfma_f32_16x16x32_f16 v[102:105], v[196:199], v[240:243], v[102:105]
	v_mfma_f32_16x16x32_f16 v[106:109], v[204:207], v[232:235], v[106:109]
	v_mfma_f32_16x16x32_f16 v[110:113], v[204:207], v[240:243], v[110:113]
	v_mfma_f32_16x16x32_f16 v[114:117], v[216:219], v[232:235], v[114:117]
	v_mfma_f32_16x16x32_f16 v[118:121], v[216:219], v[240:243], v[118:121]
	v_mfma_f32_16x16x32_f16 v[122:125], v[224:227], v[232:235], v[122:125]
	v_mfma_f32_16x16x32_f16 v[126:129], v[224:227], v[240:243], v[126:129]
	v_mfma_f32_16x16x32_f16 v[98:101], v[200:203], v[236:239], v[98:101]
	v_mfma_f32_16x16x32_f16 v[102:105], v[200:203], v[244:247], v[102:105]
	v_mfma_f32_16x16x32_f16 v[106:109], v[212:215], v[236:239], v[106:109]
	v_mfma_f32_16x16x32_f16 v[110:113], v[212:215], v[244:247], v[110:113]
	v_mfma_f32_16x16x32_f16 v[114:117], v[220:223], v[236:239], v[114:117]
	v_mfma_f32_16x16x32_f16 v[118:121], v[220:223], v[244:247], v[118:121]
	v_mfma_f32_16x16x32_f16 v[122:125], v[228:231], v[236:239], v[122:125]
	v_mfma_f32_16x16x32_f16 v[126:129], v[228:231], v[244:247], v[126:129]
	s_barrier
	ds_read_b128 v[176:179], v148
	ds_read_b128 v[184:187], v150
	ds_read_b128 v[180:183], v149
	ds_read_b128 v[188:191], v151
	v_lshl_add_u64 v[232:233], v[192:193], 0, s[36:37]
	s_mov_b32 m0, s80
	ds_read_b128 v[196:199], v173 offset:32768
	ds_read_b128 v[204:207], v173 offset:34816
	ds_read_b128 v[216:219], v173 offset:36864
	ds_read_b128 v[224:227], v173 offset:38912
	ds_read_b128 v[200:203], v173 offset:33792
	ds_read_b128 v[212:215], v173 offset:35840
	ds_read_b128 v[220:223], v173 offset:37888
	ds_read_b128 v[228:231], v173 offset:39936
	global_load_lds_dwordx4 v[232:233], off
	s_mov_b32 m0, s81
	v_lshl_add_u64 v[232:233], v[248:249], 0, s[36:37]
	global_load_lds_dwordx4 v[232:233], off
	s_waitcnt lgkmcnt(8)
	s_barrier
	s_waitcnt lgkmcnt(4)
	v_mfma_f32_16x16x32_f16 v[2:5], v[196:199], v[176:179], v[2:5]
	v_mfma_f32_16x16x32_f16 v[6:9], v[196:199], v[184:187], v[6:9]
	v_mfma_f32_16x16x32_f16 v[10:13], v[204:207], v[176:179], v[10:13]
	v_mfma_f32_16x16x32_f16 v[18:21], v[204:207], v[184:187], v[18:21]
	v_mfma_f32_16x16x32_f16 v[30:33], v[216:219], v[176:179], v[30:33]
	v_mfma_f32_16x16x32_f16 v[42:45], v[216:219], v[184:187], v[42:45]
	v_mfma_f32_16x16x32_f16 v[54:57], v[224:227], v[176:179], v[54:57]
	v_mfma_f32_16x16x32_f16 v[66:69], v[224:227], v[184:187], v[66:69]
	s_waitcnt lgkmcnt(0)
	v_mfma_f32_16x16x32_f16 v[2:5], v[200:203], v[180:183], v[2:5]
	v_mfma_f32_16x16x32_f16 v[6:9], v[200:203], v[188:191], v[6:9]
	v_mfma_f32_16x16x32_f16 v[10:13], v[212:215], v[180:183], v[10:13]
	v_mfma_f32_16x16x32_f16 v[18:21], v[212:215], v[188:191], v[18:21]
	v_mfma_f32_16x16x32_f16 v[30:33], v[220:223], v[180:183], v[30:33]
	v_mfma_f32_16x16x32_f16 v[42:45], v[220:223], v[188:191], v[42:45]
	v_mfma_f32_16x16x32_f16 v[54:57], v[228:231], v[180:183], v[54:57]
	v_mfma_f32_16x16x32_f16 v[66:69], v[228:231], v[188:191], v[66:69]
	s_barrier
	v_lshl_add_u64 v[254:255], v[250:251], 0, s[38:39]
	s_mov_b32 m0, s82
	ds_read_b128 v[232:235], v142
	ds_read_b128 v[240:243], v144
	ds_read_b128 v[236:239], v143
	ds_read_b128 v[244:247], v145
	global_load_lds_dwordx4 v[254:255], off
	s_mov_b32 m0, s83
	v_lshl_add_u64 v[254:255], v[252:253], 0, s[38:39]
	global_load_lds_dwordx4 v[254:255], off
	s_barrier
	s_waitcnt lgkmcnt(2)
	v_mfma_f32_16x16x32_f16 v[14:17], v[196:199], v[232:235], v[14:17]
	v_mfma_f32_16x16x32_f16 v[22:25], v[196:199], v[240:243], v[22:25]
	v_mfma_f32_16x16x32_f16 v[34:37], v[204:207], v[232:235], v[34:37]
	v_mfma_f32_16x16x32_f16 v[46:49], v[204:207], v[240:243], v[46:49]
	v_mfma_f32_16x16x32_f16 v[58:61], v[216:219], v[232:235], v[58:61]
	v_mfma_f32_16x16x32_f16 v[70:73], v[216:219], v[240:243], v[70:73]
	v_mfma_f32_16x16x32_f16 v[78:81], v[224:227], v[232:235], v[78:81]
	v_mfma_f32_16x16x32_f16 v[86:89], v[224:227], v[240:243], v[86:89]
	s_waitcnt lgkmcnt(0)
	v_mfma_f32_16x16x32_f16 v[14:17], v[200:203], v[236:239], v[14:17]
	v_mfma_f32_16x16x32_f16 v[22:25], v[200:203], v[244:247], v[22:25]
	v_mfma_f32_16x16x32_f16 v[34:37], v[212:215], v[236:239], v[34:37]
	v_mfma_f32_16x16x32_f16 v[46:49], v[212:215], v[244:247], v[46:49]
	v_mfma_f32_16x16x32_f16 v[58:61], v[220:223], v[236:239], v[58:61]
	v_mfma_f32_16x16x32_f16 v[70:73], v[220:223], v[244:247], v[70:73]
	v_mfma_f32_16x16x32_f16 v[78:81], v[228:231], v[236:239], v[78:81]
	v_mfma_f32_16x16x32_f16 v[86:89], v[228:231], v[244:247], v[86:89]
	v_lshl_add_u64 v[192:193], v[192:193], 0, s[38:39]
	s_mov_b32 m0, s84
	s_barrier
	ds_read_b128 v[196:199], v173 offset:49152
	ds_read_b128 v[204:207], v173 offset:51200
	ds_read_b128 v[216:219], v173 offset:53248
	ds_read_b128 v[224:227], v173 offset:55296
	ds_read_b128 v[200:203], v173 offset:50176
	ds_read_b128 v[212:215], v173 offset:52224
	ds_read_b128 v[220:223], v173 offset:54272
	ds_read_b128 v[228:231], v173 offset:56320
	global_load_lds_dwordx4 v[192:193], off
	s_mov_b32 m0, s85
	v_lshl_add_u64 v[192:193], v[248:249], 0, s[38:39]
	global_load_lds_dwordx4 v[192:193], off
	s_barrier
	s_waitcnt lgkmcnt(4)
	v_mfma_f32_16x16x32_f16 v[26:29], v[196:199], v[176:179], v[26:29]
	v_mfma_f32_16x16x32_f16 v[38:41], v[196:199], v[184:187], v[38:41]
	v_mfma_f32_16x16x32_f16 v[50:53], v[204:207], v[176:179], v[50:53]
	v_mfma_f32_16x16x32_f16 v[62:65], v[204:207], v[184:187], v[62:65]
	v_mfma_f32_16x16x32_f16 v[74:77], v[216:219], v[176:179], v[74:77]
	v_mfma_f32_16x16x32_f16 v[82:85], v[216:219], v[184:187], v[82:85]
	v_mfma_f32_16x16x32_f16 v[90:93], v[224:227], v[176:179], v[90:93]
	v_mfma_f32_16x16x32_f16 v[94:97], v[224:227], v[184:187], v[94:97]
	s_waitcnt lgkmcnt(0)
	v_mfma_f32_16x16x32_f16 v[26:29], v[200:203], v[180:183], v[26:29]
	v_mfma_f32_16x16x32_f16 v[38:41], v[200:203], v[188:191], v[38:41]
	v_mfma_f32_16x16x32_f16 v[50:53], v[212:215], v[180:183], v[50:53]
	v_mfma_f32_16x16x32_f16 v[62:65], v[212:215], v[188:191], v[62:65]
	v_mfma_f32_16x16x32_f16 v[74:77], v[220:223], v[180:183], v[74:77]
	v_mfma_f32_16x16x32_f16 v[82:85], v[220:223], v[188:191], v[82:85]
	v_mfma_f32_16x16x32_f16 v[90:93], v[228:231], v[180:183], v[90:93]
	v_mfma_f32_16x16x32_f16 v[94:97], v[228:231], v[188:191], v[94:97]
	s_barrier
	s_mov_b32 m0, s86
	v_lshl_add_u64 v[176:177], v[250:251], 0, s[40:41]
	global_load_lds_dwordx4 v[176:177], off
	s_mov_b32 m0, s87
	v_lshl_add_u64 v[176:177], v[252:253], 0, s[40:41]
	global_load_lds_dwordx4 v[176:177], off
	s_waitcnt vmcnt(6)
	s_barrier
	v_mfma_f32_16x16x32_f16 v[98:101], v[196:199], v[232:235], v[98:101]
	v_mfma_f32_16x16x32_f16 v[102:105], v[196:199], v[240:243], v[102:105]
	v_mfma_f32_16x16x32_f16 v[106:109], v[204:207], v[232:235], v[106:109]
	v_mfma_f32_16x16x32_f16 v[110:113], v[204:207], v[240:243], v[110:113]
	v_mfma_f32_16x16x32_f16 v[114:117], v[216:219], v[232:235], v[114:117]
	v_mfma_f32_16x16x32_f16 v[118:121], v[216:219], v[240:243], v[118:121]
	v_mfma_f32_16x16x32_f16 v[122:125], v[224:227], v[232:235], v[122:125]
	v_mfma_f32_16x16x32_f16 v[126:129], v[224:227], v[240:243], v[126:129]
	v_mfma_f32_16x16x32_f16 v[98:101], v[200:203], v[236:239], v[98:101]
	v_mfma_f32_16x16x32_f16 v[102:105], v[200:203], v[244:247], v[102:105]
	v_mfma_f32_16x16x32_f16 v[106:109], v[212:215], v[236:239], v[106:109]
	v_mfma_f32_16x16x32_f16 v[110:113], v[212:215], v[244:247], v[110:113]
	v_mfma_f32_16x16x32_f16 v[114:117], v[220:223], v[236:239], v[114:117]
	v_mfma_f32_16x16x32_f16 v[118:121], v[220:223], v[244:247], v[118:121]
	v_mfma_f32_16x16x32_f16 v[122:125], v[228:231], v[236:239], v[122:125]
	v_mfma_f32_16x16x32_f16 v[126:129], v[228:231], v[244:247], v[126:129]
	s_add_i32 s46, s46, 2
	s_add_u32 s44, s44, 0x100
	s_addc_u32 s45, s45, 0
	s_cmp_lt_u32 s46, 4
	s_barrier
	s_cbranch_scc1 .LBB6_12
	s_add_u32 s0, s0, 0x20380
	s_addc_u32 s1, s1, 0
	v_readfirstlane_b32 s17, v174
	v_lshl_add_u64 v[130:131], v[130:131], 1, s[0:1]
	s_mov_b32 m0, s17
	ds_read_b128 v[134:137], v169
	ds_read_b128 v[138:141], v170
	ds_read_b128 v[152:155], v171
	ds_read_b128 v[156:159], v172
	ds_read_b128 v[166:169], v173
	ds_read_b128 v[176:179], v173 offset:1024
	ds_read_b128 v[180:183], v173 offset:2048
	ds_read_b128 v[184:187], v173 offset:3072
	ds_read_b128 v[188:191], v173 offset:4096
	ds_read_b128 v[196:199], v173 offset:5120
	ds_read_b128 v[200:203], v173 offset:6144
	ds_read_b128 v[204:207], v173 offset:7168
	global_load_lds_dwordx4 v[130:131], off
	v_lshl_add_u64 v[130:131], v[132:133], 1, s[0:1]
	v_readfirstlane_b32 s0, v175
	s_mov_b32 m0, s0
	s_nop 0
	global_load_lds_dwordx4 v[130:131], off
	s_barrier
	s_waitcnt lgkmcnt(0)
	v_mfma_f32_16x16x32_f16 v[2:5], v[166:169], v[134:137], v[2:5]
	v_mfma_f32_16x16x32_f16 v[42:45], v[188:191], v[152:155], v[42:45]
	v_mfma_f32_16x16x32_f16 v[54:57], v[200:203], v[134:137], v[54:57]
	v_mfma_f32_16x16x32_f16 v[66:69], v[200:203], v[152:155], v[66:69]
	v_mfma_f32_16x16x32_f16 v[2:5], v[176:179], v[138:141], v[2:5]
	v_mfma_f32_16x16x32_f16 v[6:9], v[166:169], v[152:155], v[6:9]
	v_mfma_f32_16x16x32_f16 v[10:13], v[180:183], v[134:137], v[10:13]
	v_mfma_f32_16x16x32_f16 v[18:21], v[180:183], v[152:155], v[18:21]
	v_mfma_f32_16x16x32_f16 v[30:33], v[188:191], v[134:137], v[30:33]
	v_mfma_f32_16x16x32_f16 v[42:45], v[196:199], v[156:159], v[42:45]
	v_mfma_f32_16x16x32_f16 v[54:57], v[204:207], v[138:141], v[54:57]
	v_mfma_f32_16x16x32_f16 v[66:69], v[204:207], v[156:159], v[66:69]
	v_mfma_f32_16x16x32_f16 v[6:9], v[176:179], v[156:159], v[6:9]
	v_mfma_f32_16x16x32_f16 v[10:13], v[184:187], v[138:141], v[10:13]
	v_mfma_f32_16x16x32_f16 v[18:21], v[184:187], v[156:159], v[18:21]
	v_mfma_f32_16x16x32_f16 v[30:33], v[196:199], v[138:141], v[30:33]
	s_barrier
	ds_read_b128 v[130:133], v161
	ds_read_b128 v[212:215], v162
	ds_read_b128 v[160:163], v163
	ds_read_b128 v[216:219], v164
	s_barrier
	s_waitcnt lgkmcnt(0)
	v_mfma_f32_16x16x32_f16 v[14:17], v[166:169], v[130:133], v[14:17]
	v_mfma_f32_16x16x32_f16 v[78:81], v[200:203], v[130:133], v[78:81]
	v_mfma_f32_16x16x32_f16 v[14:17], v[176:179], v[212:215], v[14:17]
	v_mfma_f32_16x16x32_f16 v[22:25], v[166:169], v[160:163], v[22:25]
	v_mfma_f32_16x16x32_f16 v[34:37], v[180:183], v[130:133], v[34:37]
	v_mfma_f32_16x16x32_f16 v[46:49], v[180:183], v[160:163], v[46:49]
	v_mfma_f32_16x16x32_f16 v[58:61], v[188:191], v[130:133], v[58:61]
	v_mfma_f32_16x16x32_f16 v[70:73], v[188:191], v[160:163], v[70:73]
	v_mfma_f32_16x16x32_f16 v[164:167], v[204:207], v[212:215], v[78:81]
	v_mfma_f32_16x16x32_f16 v[78:81], v[200:203], v[160:163], v[86:89]
	v_mfma_f32_16x16x32_f16 v[22:25], v[176:179], v[216:219], v[22:25]
	v_mfma_f32_16x16x32_f16 v[34:37], v[184:187], v[212:215], v[34:37]
	v_mfma_f32_16x16x32_f16 v[46:49], v[184:187], v[216:219], v[46:49]
	v_mfma_f32_16x16x32_f16 v[58:61], v[196:199], v[212:215], v[58:61]
	v_mfma_f32_16x16x32_f16 v[70:73], v[196:199], v[216:219], v[70:73]
	v_mfma_f32_16x16x32_f16 v[86:89], v[204:207], v[216:219], v[78:81]
	s_barrier
	s_nop 0
	ds_read_b128 v[78:81], v173 offset:16384
	ds_read_b128 v[168:171], v173 offset:17408
	ds_read_b128 v[174:177], v173 offset:18432
	ds_read_b128 v[178:181], v173 offset:19456
	ds_read_b128 v[182:185], v173 offset:20480
	ds_read_b128 v[186:189], v173 offset:21504
	ds_read_b128 v[190:193], v173 offset:22528
	ds_read_b128 v[196:199], v173 offset:23552
	s_waitcnt vmcnt(4)
	s_barrier
	s_waitcnt lgkmcnt(0)
	v_mfma_f32_16x16x32_f16 v[26:29], v[78:81], v[134:137], v[26:29]
	v_mfma_f32_16x16x32_f16 v[38:41], v[78:81], v[152:155], v[38:41]
	v_mfma_f32_16x16x32_f16 v[26:29], v[168:171], v[138:141], v[26:29]
	v_mfma_f32_16x16x32_f16 v[38:41], v[168:171], v[156:159], v[38:41]
	v_mfma_f32_16x16x32_f16 v[50:53], v[174:177], v[134:137], v[50:53]
	v_mfma_f32_16x16x32_f16 v[62:65], v[174:177], v[152:155], v[62:65]
	v_mfma_f32_16x16x32_f16 v[74:77], v[182:185], v[134:137], v[74:77]
	v_mfma_f32_16x16x32_f16 v[82:85], v[182:185], v[152:155], v[82:85]
	v_mfma_f32_16x16x32_f16 v[90:93], v[190:193], v[134:137], v[90:93]
	v_mfma_f32_16x16x32_f16 v[94:97], v[190:193], v[152:155], v[94:97]
	v_mfma_f32_16x16x32_f16 v[50:53], v[178:181], v[138:141], v[50:53]
	v_mfma_f32_16x16x32_f16 v[62:65], v[178:181], v[156:159], v[62:65]
	v_mfma_f32_16x16x32_f16 v[74:77], v[186:189], v[138:141], v[74:77]
	v_mfma_f32_16x16x32_f16 v[82:85], v[186:189], v[156:159], v[82:85]
	v_mfma_f32_16x16x32_f16 v[90:93], v[196:199], v[138:141], v[90:93]
	v_mfma_f32_16x16x32_f16 v[94:97], v[196:199], v[156:159], v[94:97]
	v_mfma_f32_16x16x32_f16 v[98:101], v[78:81], v[130:133], v[98:101]
	v_mfma_f32_16x16x32_f16 v[78:81], v[78:81], v[160:163], v[102:105]
	v_mfma_f32_16x16x32_f16 v[102:105], v[168:171], v[216:219], v[78:81]
	v_mfma_f32_16x16x32_f16 v[78:81], v[174:177], v[130:133], v[106:109]
	v_mfma_f32_16x16x32_f16 v[106:109], v[178:181], v[212:215], v[78:81]
	v_mfma_f32_16x16x32_f16 v[78:81], v[174:177], v[160:163], v[110:113]
	v_mfma_f32_16x16x32_f16 v[200:203], v[178:181], v[216:219], v[78:81]
	v_mfma_f32_16x16x32_f16 v[78:81], v[182:185], v[130:133], v[114:117]
	v_mfma_f32_16x16x32_f16 v[204:207], v[186:189], v[212:215], v[78:81]
	v_mfma_f32_16x16x32_f16 v[78:81], v[182:185], v[160:163], v[118:121]
	v_mfma_f32_16x16x32_f16 v[220:223], v[186:189], v[216:219], v[78:81]
	v_mfma_f32_16x16x32_f16 v[78:81], v[190:193], v[130:133], v[122:125]
	v_mfma_f32_16x16x32_f16 v[98:101], v[168:171], v[212:215], v[98:101]
	v_mfma_f32_16x16x32_f16 v[212:215], v[196:199], v[212:215], v[78:81]
	v_mfma_f32_16x16x32_f16 v[78:81], v[190:193], v[160:163], v[126:129]
	v_mfma_f32_16x16x32_f16 v[196:199], v[196:199], v[216:219], v[78:81]
	s_barrier
	ds_read_b128 v[110:113], v148
	ds_read_b128 v[130:133], v149
	ds_read_b128 v[216:219], v150
	ds_read_b128 v[224:227], v151
	s_nop 0
	ds_read_b128 v[78:81], v173 offset:32768
	ds_read_b128 v[114:117], v173 offset:33792
	ds_read_b128 v[118:121], v173 offset:34816
	ds_read_b128 v[134:137], v173 offset:35840
	ds_read_b128 v[138:141], v173 offset:36864
	ds_read_b128 v[168:171], v173 offset:37888
	ds_read_b128 v[174:177], v173 offset:38912
	ds_read_b128 v[228:231], v173 offset:39936
	s_waitcnt vmcnt(2)
	s_barrier
	s_waitcnt lgkmcnt(0)
	v_mfma_f32_16x16x32_f16 v[2:5], v[78:81], v[110:113], v[2:5]
	v_mfma_f32_16x16x32_f16 v[190:193], v[114:117], v[130:133], v[2:5]
	v_mfma_f32_16x16x32_f16 v[2:5], v[78:81], v[216:219], v[6:9]
	v_mfma_f32_16x16x32_f16 v[158:161], v[114:117], v[224:227], v[2:5]
	v_mfma_f32_16x16x32_f16 v[2:5], v[118:121], v[110:113], v[10:13]
	v_mfma_f32_16x16x32_f16 v[186:189], v[134:137], v[130:133], v[2:5]
	v_mfma_f32_16x16x32_f16 v[2:5], v[118:121], v[216:219], v[18:21]
	v_mfma_f32_16x16x32_f16 v[154:157], v[134:137], v[224:227], v[2:5]
	v_mfma_f32_16x16x32_f16 v[2:5], v[138:141], v[110:113], v[30:33]
	v_mfma_f32_16x16x32_f16 v[182:185], v[168:171], v[130:133], v[2:5]
	v_mfma_f32_16x16x32_f16 v[2:5], v[138:141], v[216:219], v[42:45]
	v_mfma_f32_16x16x32_f16 v[150:153], v[168:171], v[224:227], v[2:5]
	v_mfma_f32_16x16x32_f16 v[2:5], v[174:177], v[110:113], v[54:57]
	v_mfma_f32_16x16x32_f16 v[178:181], v[228:231], v[130:133], v[2:5]
	v_mfma_f32_16x16x32_f16 v[2:5], v[174:177], v[216:219], v[66:69]
	v_mfma_f32_16x16x32_f16 v[146:149], v[228:231], v[224:227], v[2:5]
	s_barrier
	s_nop 4
	ds_read_b128 v[2:5], v142
	ds_read_b128 v[6:9], v143
	ds_read_b128 v[10:13], v144
	ds_read_b128 v[18:21], v145
	s_waitcnt vmcnt(0)
	s_barrier
	s_waitcnt lgkmcnt(0)
	v_mfma_f32_16x16x32_f16 v[14:17], v[78:81], v[2:5], v[14:17]
	v_mfma_f32_16x16x32_f16 v[126:129], v[114:117], v[6:9], v[14:17]
	v_mfma_f32_16x16x32_f16 v[14:17], v[78:81], v[10:13], v[22:25]
	v_mfma_f32_16x16x32_f16 v[78:81], v[114:117], v[18:21], v[14:17]
	v_mfma_f32_16x16x32_f16 v[14:17], v[118:121], v[2:5], v[34:37]
	v_mfma_f32_16x16x32_f16 v[122:125], v[134:137], v[6:9], v[14:17]
	v_mfma_f32_16x16x32_f16 v[14:17], v[118:121], v[10:13], v[46:49]
	v_mfma_f32_16x16x32_f16 v[66:69], v[134:137], v[18:21], v[14:17]
	v_mfma_f32_16x16x32_f16 v[14:17], v[138:141], v[2:5], v[58:61]
	v_mfma_f32_16x16x32_f16 v[118:121], v[168:171], v[6:9], v[14:17]
	v_mfma_f32_16x16x32_f16 v[14:17], v[138:141], v[10:13], v[70:73]
	v_mfma_f32_16x16x32_f16 v[54:57], v[168:171], v[18:21], v[14:17]
	v_mfma_f32_16x16x32_f16 v[14:17], v[174:177], v[2:5], v[164:167]
	v_mfma_f32_16x16x32_f16 v[114:117], v[228:231], v[6:9], v[14:17]
	v_mfma_f32_16x16x32_f16 v[14:17], v[174:177], v[10:13], v[86:89]
	v_mfma_f32_16x16x32_f16 v[42:45], v[228:231], v[18:21], v[14:17]
	s_barrier
	s_nop 4
	ds_read_b128 v[14:17], v173 offset:49152
	ds_read_b128 v[22:25], v173 offset:50176
	ds_read_b128 v[30:33], v173 offset:51200
	ds_read_b128 v[34:37], v173 offset:52224
	ds_read_b128 v[46:49], v173 offset:53248
	ds_read_b128 v[58:61], v173 offset:54272
	ds_read_b128 v[70:73], v173 offset:55296
	ds_read_b128 v[86:89], v173 offset:56320
	s_barrier
	s_waitcnt lgkmcnt(0)
	v_mfma_f32_16x16x32_f16 v[26:29], v[14:17], v[110:113], v[26:29]
	v_mfma_f32_16x16x32_f16 v[174:177], v[22:25], v[130:133], v[26:29]
	v_mfma_f32_16x16x32_f16 v[26:29], v[14:17], v[216:219], v[38:41]
	v_mfma_f32_16x16x32_f16 v[142:145], v[22:25], v[224:227], v[26:29]
	v_mfma_f32_16x16x32_f16 v[26:29], v[30:33], v[110:113], v[50:53]
	v_mfma_f32_16x16x32_f16 v[170:173], v[34:37], v[130:133], v[26:29]
	v_mfma_f32_16x16x32_f16 v[26:29], v[30:33], v[216:219], v[62:65]
	v_mfma_f32_16x16x32_f16 v[138:141], v[34:37], v[224:227], v[26:29]
	v_mfma_f32_16x16x32_f16 v[26:29], v[46:49], v[110:113], v[74:77]
	v_mfma_f32_16x16x32_f16 v[166:169], v[58:61], v[130:133], v[26:29]
	v_mfma_f32_16x16x32_f16 v[26:29], v[46:49], v[216:219], v[82:85]
	v_mfma_f32_16x16x32_f16 v[134:137], v[58:61], v[224:227], v[26:29]
	v_mfma_f32_16x16x32_f16 v[26:29], v[70:73], v[110:113], v[90:93]
	v_mfma_f32_16x16x32_f16 v[162:165], v[86:89], v[130:133], v[26:29]
	v_mfma_f32_16x16x32_f16 v[26:29], v[70:73], v[216:219], v[94:97]
	v_mfma_f32_16x16x32_f16 v[130:133], v[86:89], v[224:227], v[26:29]
	v_mfma_f32_16x16x32_f16 v[26:29], v[14:17], v[2:5], v[98:101]
	v_mfma_f32_16x16x32_f16 v[14:17], v[14:17], v[10:13], v[102:105]
	v_mfma_f32_16x16x32_f16 v[38:41], v[22:25], v[18:21], v[14:17]
	v_mfma_f32_16x16x32_f16 v[14:17], v[30:33], v[2:5], v[106:109]
	v_mfma_f32_16x16x32_f16 v[106:109], v[34:37], v[6:9], v[14:17]
	v_mfma_f32_16x16x32_f16 v[14:17], v[30:33], v[10:13], v[200:203]
	v_mfma_f32_16x16x32_f16 v[110:113], v[22:25], v[6:9], v[26:29]
	v_mfma_f32_16x16x32_f16 v[26:29], v[34:37], v[18:21], v[14:17]
	v_mfma_f32_16x16x32_f16 v[14:17], v[46:49], v[2:5], v[204:207]
	v_mfma_f32_16x16x32_f16 v[2:5], v[70:73], v[2:5], v[212:215]
	v_mfma_f32_16x16x32_f16 v[102:105], v[58:61], v[6:9], v[14:17]
	v_mfma_f32_16x16x32_f16 v[14:17], v[46:49], v[10:13], v[220:223]
	v_mfma_f32_16x16x32_f16 v[98:101], v[86:89], v[6:9], v[2:5]
	v_mfma_f32_16x16x32_f16 v[2:5], v[70:73], v[10:13], v[196:199]
	v_mfma_f32_16x16x32_f16 v[14:17], v[58:61], v[18:21], v[14:17]
	v_mfma_f32_16x16x32_f16 v[2:5], v[86:89], v[18:21], v[2:5]
	s_cmpk_gt_u32 s65, 0xff
	s_barrier
	s_cbranch_scc1 .LBB6_15
	s_barrier

.LBB7_239:
	ds_read_b128 v[176:179], v169
	ds_read_b128 v[184:187], v171
	ds_read_b128 v[180:183], v170
	ds_read_b128 v[188:191], v172
	v_add_u32_e32 v174, 0xc000, v152
	v_lshl_add_u64 v[192:193], v[136:137], 0, s[46:47]
	v_add_u32_e32 v175, 0xe000, v152
	v_add_u32_e32 v173, s5, v168
	v_lshl_add_u64 v[232:233], v[192:193], 0, s[34:35]
	s_mov_b32 m0, s72
	v_lshl_add_u64 v[248:249], v[134:135], 0, s[46:47]
	ds_read_b128 v[196:199], v173
	ds_read_b128 v[204:207], v173 offset:2048
	ds_read_b128 v[216:219], v173 offset:4096
	ds_read_b128 v[224:227], v173 offset:6144
	ds_read_b128 v[200:203], v173 offset:1024
	ds_read_b128 v[212:215], v173 offset:3072
	ds_read_b128 v[220:223], v173 offset:5120
	ds_read_b128 v[228:231], v173 offset:7168
	global_load_lds_dwordx4 v[232:233], off
	s_mov_b32 m0, s73
	v_lshl_add_u64 v[232:233], v[248:249], 0, s[34:35]
	global_load_lds_dwordx4 v[232:233], off
	s_waitcnt lgkmcnt(8)
	s_barrier
	s_waitcnt lgkmcnt(4)
	v_mfma_f32_16x16x32_f16 v[2:5], v[196:199], v[176:179], v[2:5]
	v_mfma_f32_16x16x32_f16 v[6:9], v[196:199], v[184:187], v[6:9]
	v_mfma_f32_16x16x32_f16 v[10:13], v[204:207], v[176:179], v[10:13]
	v_mfma_f32_16x16x32_f16 v[18:21], v[204:207], v[184:187], v[18:21]
	v_mfma_f32_16x16x32_f16 v[30:33], v[216:219], v[176:179], v[30:33]
	v_mfma_f32_16x16x32_f16 v[42:45], v[216:219], v[184:187], v[42:45]
	v_mfma_f32_16x16x32_f16 v[54:57], v[224:227], v[176:179], v[54:57]
	v_mfma_f32_16x16x32_f16 v[66:69], v[224:227], v[184:187], v[66:69]
	s_waitcnt lgkmcnt(0)
	v_mfma_f32_16x16x32_f16 v[2:5], v[200:203], v[180:183], v[2:5]
	v_mfma_f32_16x16x32_f16 v[6:9], v[200:203], v[188:191], v[6:9]
	v_mfma_f32_16x16x32_f16 v[10:13], v[212:215], v[180:183], v[10:13]
	v_mfma_f32_16x16x32_f16 v[18:21], v[212:215], v[188:191], v[18:21]
	v_mfma_f32_16x16x32_f16 v[30:33], v[220:223], v[180:183], v[30:33]
	v_mfma_f32_16x16x32_f16 v[42:45], v[220:223], v[188:191], v[42:45]
	v_mfma_f32_16x16x32_f16 v[54:57], v[228:231], v[180:183], v[54:57]
	v_mfma_f32_16x16x32_f16 v[66:69], v[228:231], v[188:191], v[66:69]
	s_barrier
	v_lshl_add_u64 v[250:251], v[140:141], 0, s[46:47]
	v_lshl_add_u64 v[252:253], v[250:251], 0, s[36:37]
	s_mov_b32 m0, s74
	ds_read_b128 v[232:235], v161
	ds_read_b128 v[240:243], v163
	ds_read_b128 v[236:239], v162
	ds_read_b128 v[244:247], v164
	global_load_lds_dwordx4 v[252:253], off
	v_lshl_add_u64 v[252:253], v[138:139], 0, s[46:47]
	s_mov_b32 m0, s75
	v_lshl_add_u64 v[254:255], v[252:253], 0, s[36:37]
	global_load_lds_dwordx4 v[254:255], off
	s_barrier
	s_waitcnt lgkmcnt(2)
	v_mfma_f32_16x16x32_f16 v[14:17], v[196:199], v[232:235], v[14:17]
	v_mfma_f32_16x16x32_f16 v[22:25], v[196:199], v[240:243], v[22:25]
	v_mfma_f32_16x16x32_f16 v[34:37], v[204:207], v[232:235], v[34:37]
	v_mfma_f32_16x16x32_f16 v[46:49], v[204:207], v[240:243], v[46:49]
	v_mfma_f32_16x16x32_f16 v[58:61], v[216:219], v[232:235], v[58:61]
	v_mfma_f32_16x16x32_f16 v[70:73], v[216:219], v[240:243], v[70:73]
	v_mfma_f32_16x16x32_f16 v[78:81], v[224:227], v[232:235], v[78:81]
	v_mfma_f32_16x16x32_f16 v[86:89], v[224:227], v[240:243], v[86:89]
	s_waitcnt lgkmcnt(0)
	v_mfma_f32_16x16x32_f16 v[14:17], v[200:203], v[236:239], v[14:17]
	v_mfma_f32_16x16x32_f16 v[22:25], v[200:203], v[244:247], v[22:25]
	v_mfma_f32_16x16x32_f16 v[34:37], v[212:215], v[236:239], v[34:37]
	v_mfma_f32_16x16x32_f16 v[46:49], v[212:215], v[244:247], v[46:49]
	v_mfma_f32_16x16x32_f16 v[58:61], v[220:223], v[236:239], v[58:61]
	v_mfma_f32_16x16x32_f16 v[70:73], v[220:223], v[244:247], v[70:73]
	v_mfma_f32_16x16x32_f16 v[78:81], v[228:231], v[236:239], v[78:81]
	v_mfma_f32_16x16x32_f16 v[86:89], v[228:231], v[244:247], v[86:89]
	v_lshl_add_u64 v[254:255], v[192:193], 0, s[36:37]
	s_mov_b32 m0, s76
	s_barrier
	ds_read_b128 v[196:199], v173 offset:16384
	ds_read_b128 v[204:207], v173 offset:18432
	ds_read_b128 v[216:219], v173 offset:20480
	ds_read_b128 v[224:227], v173 offset:22528
	ds_read_b128 v[200:203], v173 offset:17408
	ds_read_b128 v[212:215], v173 offset:19456
	ds_read_b128 v[220:223], v173 offset:21504
	ds_read_b128 v[228:231], v173 offset:23552
	global_load_lds_dwordx4 v[254:255], off
	s_mov_b32 m0, s77
	v_lshl_add_u64 v[254:255], v[248:249], 0, s[36:37]
	global_load_lds_dwordx4 v[254:255], off
	s_barrier
	s_waitcnt lgkmcnt(4)
	v_mfma_f32_16x16x32_f16 v[26:29], v[196:199], v[176:179], v[26:29]
	v_mfma_f32_16x16x32_f16 v[38:41], v[196:199], v[184:187], v[38:41]
	v_mfma_f32_16x16x32_f16 v[50:53], v[204:207], v[176:179], v[50:53]
	v_mfma_f32_16x16x32_f16 v[62:65], v[204:207], v[184:187], v[62:65]
	v_mfma_f32_16x16x32_f16 v[74:77], v[216:219], v[176:179], v[74:77]
	v_mfma_f32_16x16x32_f16 v[82:85], v[216:219], v[184:187], v[82:85]
	v_mfma_f32_16x16x32_f16 v[90:93], v[224:227], v[176:179], v[90:93]
	v_mfma_f32_16x16x32_f16 v[94:97], v[224:227], v[184:187], v[94:97]
	s_waitcnt lgkmcnt(0)
	v_mfma_f32_16x16x32_f16 v[26:29], v[200:203], v[180:183], v[26:29]
	v_mfma_f32_16x16x32_f16 v[38:41], v[200:203], v[188:191], v[38:41]
	v_mfma_f32_16x16x32_f16 v[50:53], v[212:215], v[180:183], v[50:53]
	v_mfma_f32_16x16x32_f16 v[62:65], v[212:215], v[188:191], v[62:65]
	v_mfma_f32_16x16x32_f16 v[74:77], v[220:223], v[180:183], v[74:77]
	v_mfma_f32_16x16x32_f16 v[82:85], v[220:223], v[188:191], v[82:85]
	v_mfma_f32_16x16x32_f16 v[90:93], v[228:231], v[180:183], v[90:93]
	v_mfma_f32_16x16x32_f16 v[94:97], v[228:231], v[188:191], v[94:97]
	s_barrier
	s_mov_b32 m0, s78
	v_lshl_add_u64 v[176:177], v[250:251], 0, s[38:39]
	global_load_lds_dwordx4 v[176:177], off
	s_mov_b32 m0, s79
	v_lshl_add_u64 v[176:177], v[252:253], 0, s[38:39]
	global_load_lds_dwordx4 v[176:177], off
	s_waitcnt vmcnt(6)
	s_barrier
	v_mfma_f32_16x16x32_f16 v[98:101], v[196:199], v[232:235], v[98:101]
	v_mfma_f32_16x16x32_f16 v[102:105], v[196:199], v[240:243], v[102:105]
	v_mfma_f32_16x16x32_f16 v[106:109], v[204:207], v[232:235], v[106:109]
	v_mfma_f32_16x16x32_f16 v[110:113], v[204:207], v[240:243], v[110:113]
	v_mfma_f32_16x16x32_f16 v[114:117], v[216:219], v[232:235], v[114:117]
	v_mfma_f32_16x16x32_f16 v[118:121], v[216:219], v[240:243], v[118:121]
	v_mfma_f32_16x16x32_f16 v[122:125], v[224:227], v[232:235], v[122:125]
	v_mfma_f32_16x16x32_f16 v[126:129], v[224:227], v[240:243], v[126:129]
	v_mfma_f32_16x16x32_f16 v[98:101], v[200:203], v[236:239], v[98:101]
	v_mfma_f32_16x16x32_f16 v[102:105], v[200:203], v[244:247], v[102:105]
	v_mfma_f32_16x16x32_f16 v[106:109], v[212:215], v[236:239], v[106:109]
	v_mfma_f32_16x16x32_f16 v[110:113], v[212:215], v[244:247], v[110:113]
	v_mfma_f32_16x16x32_f16 v[114:117], v[220:223], v[236:239], v[114:117]
	v_mfma_f32_16x16x32_f16 v[118:121], v[220:223], v[244:247], v[118:121]
	v_mfma_f32_16x16x32_f16 v[122:125], v[228:231], v[236:239], v[122:125]
	v_mfma_f32_16x16x32_f16 v[126:129], v[228:231], v[244:247], v[126:129]
	s_barrier
	ds_read_b128 v[176:179], v148
	ds_read_b128 v[184:187], v150
	ds_read_b128 v[180:183], v149
	ds_read_b128 v[188:191], v151
	v_lshl_add_u64 v[232:233], v[192:193], 0, s[38:39]
	s_mov_b32 m0, s80
	ds_read_b128 v[196:199], v173 offset:32768
	ds_read_b128 v[204:207], v173 offset:34816
	ds_read_b128 v[216:219], v173 offset:36864
	ds_read_b128 v[224:227], v173 offset:38912
	ds_read_b128 v[200:203], v173 offset:33792
	ds_read_b128 v[212:215], v173 offset:35840
	ds_read_b128 v[220:223], v173 offset:37888
	ds_read_b128 v[228:231], v173 offset:39936
	global_load_lds_dwordx4 v[232:233], off
	s_mov_b32 m0, s81
	v_lshl_add_u64 v[232:233], v[248:249], 0, s[38:39]
	global_load_lds_dwordx4 v[232:233], off
	s_waitcnt lgkmcnt(8)
	s_barrier
	s_waitcnt lgkmcnt(4)
	v_mfma_f32_16x16x32_f16 v[2:5], v[196:199], v[176:179], v[2:5]
	v_mfma_f32_16x16x32_f16 v[6:9], v[196:199], v[184:187], v[6:9]
	v_mfma_f32_16x16x32_f16 v[10:13], v[204:207], v[176:179], v[10:13]
	v_mfma_f32_16x16x32_f16 v[18:21], v[204:207], v[184:187], v[18:21]
	v_mfma_f32_16x16x32_f16 v[30:33], v[216:219], v[176:179], v[30:33]
	v_mfma_f32_16x16x32_f16 v[42:45], v[216:219], v[184:187], v[42:45]
	v_mfma_f32_16x16x32_f16 v[54:57], v[224:227], v[176:179], v[54:57]
	v_mfma_f32_16x16x32_f16 v[66:69], v[224:227], v[184:187], v[66:69]
	s_waitcnt lgkmcnt(0)
	v_mfma_f32_16x16x32_f16 v[2:5], v[200:203], v[180:183], v[2:5]
	v_mfma_f32_16x16x32_f16 v[6:9], v[200:203], v[188:191], v[6:9]
	v_mfma_f32_16x16x32_f16 v[10:13], v[212:215], v[180:183], v[10:13]
	v_mfma_f32_16x16x32_f16 v[18:21], v[212:215], v[188:191], v[18:21]
	v_mfma_f32_16x16x32_f16 v[30:33], v[220:223], v[180:183], v[30:33]
	v_mfma_f32_16x16x32_f16 v[42:45], v[220:223], v[188:191], v[42:45]
	v_mfma_f32_16x16x32_f16 v[54:57], v[228:231], v[180:183], v[54:57]
	v_mfma_f32_16x16x32_f16 v[66:69], v[228:231], v[188:191], v[66:69]
	s_barrier
	v_lshl_add_u64 v[254:255], v[250:251], 0, s[40:41]
	s_mov_b32 m0, s82
	ds_read_b128 v[232:235], v142
	ds_read_b128 v[240:243], v144
	ds_read_b128 v[236:239], v143
	ds_read_b128 v[244:247], v145
	global_load_lds_dwordx4 v[254:255], off
	s_mov_b32 m0, s83
	v_lshl_add_u64 v[254:255], v[252:253], 0, s[40:41]
	global_load_lds_dwordx4 v[254:255], off
	s_barrier
	s_waitcnt lgkmcnt(2)
	v_mfma_f32_16x16x32_f16 v[14:17], v[196:199], v[232:235], v[14:17]
	v_mfma_f32_16x16x32_f16 v[22:25], v[196:199], v[240:243], v[22:25]
	v_mfma_f32_16x16x32_f16 v[34:37], v[204:207], v[232:235], v[34:37]
	v_mfma_f32_16x16x32_f16 v[46:49], v[204:207], v[240:243], v[46:49]
	v_mfma_f32_16x16x32_f16 v[58:61], v[216:219], v[232:235], v[58:61]
	v_mfma_f32_16x16x32_f16 v[70:73], v[216:219], v[240:243], v[70:73]
	v_mfma_f32_16x16x32_f16 v[78:81], v[224:227], v[232:235], v[78:81]
	v_mfma_f32_16x16x32_f16 v[86:89], v[224:227], v[240:243], v[86:89]
	s_waitcnt lgkmcnt(0)
	v_mfma_f32_16x16x32_f16 v[14:17], v[200:203], v[236:239], v[14:17]
	v_mfma_f32_16x16x32_f16 v[22:25], v[200:203], v[244:247], v[22:25]
	v_mfma_f32_16x16x32_f16 v[34:37], v[212:215], v[236:239], v[34:37]
	v_mfma_f32_16x16x32_f16 v[46:49], v[212:215], v[244:247], v[46:49]
	v_mfma_f32_16x16x32_f16 v[58:61], v[220:223], v[236:239], v[58:61]
	v_mfma_f32_16x16x32_f16 v[70:73], v[220:223], v[244:247], v[70:73]
	v_mfma_f32_16x16x32_f16 v[78:81], v[228:231], v[236:239], v[78:81]
	v_mfma_f32_16x16x32_f16 v[86:89], v[228:231], v[244:247], v[86:89]
	v_lshl_add_u64 v[192:193], v[192:193], 0, s[40:41]
	s_mov_b32 m0, s84
	s_barrier
	ds_read_b128 v[196:199], v173 offset:49152
	ds_read_b128 v[204:207], v173 offset:51200
	ds_read_b128 v[216:219], v173 offset:53248
	ds_read_b128 v[224:227], v173 offset:55296
	ds_read_b128 v[200:203], v173 offset:50176
	ds_read_b128 v[212:215], v173 offset:52224
	ds_read_b128 v[220:223], v173 offset:54272
	ds_read_b128 v[228:231], v173 offset:56320
	global_load_lds_dwordx4 v[192:193], off
	s_mov_b32 m0, s85
	v_lshl_add_u64 v[192:193], v[248:249], 0, s[40:41]
	global_load_lds_dwordx4 v[192:193], off
	s_barrier
	s_waitcnt lgkmcnt(4)
	v_mfma_f32_16x16x32_f16 v[26:29], v[196:199], v[176:179], v[26:29]
	v_mfma_f32_16x16x32_f16 v[38:41], v[196:199], v[184:187], v[38:41]
	v_mfma_f32_16x16x32_f16 v[50:53], v[204:207], v[176:179], v[50:53]
	v_mfma_f32_16x16x32_f16 v[62:65], v[204:207], v[184:187], v[62:65]
	v_mfma_f32_16x16x32_f16 v[74:77], v[216:219], v[176:179], v[74:77]
	v_mfma_f32_16x16x32_f16 v[82:85], v[216:219], v[184:187], v[82:85]
	v_mfma_f32_16x16x32_f16 v[90:93], v[224:227], v[176:179], v[90:93]
	v_mfma_f32_16x16x32_f16 v[94:97], v[224:227], v[184:187], v[94:97]
	s_waitcnt lgkmcnt(0)
	v_mfma_f32_16x16x32_f16 v[26:29], v[200:203], v[180:183], v[26:29]
	v_mfma_f32_16x16x32_f16 v[38:41], v[200:203], v[188:191], v[38:41]
	v_mfma_f32_16x16x32_f16 v[50:53], v[212:215], v[180:183], v[50:53]
	v_mfma_f32_16x16x32_f16 v[62:65], v[212:215], v[188:191], v[62:65]
	v_mfma_f32_16x16x32_f16 v[74:77], v[220:223], v[180:183], v[74:77]
	v_mfma_f32_16x16x32_f16 v[82:85], v[220:223], v[188:191], v[82:85]
	v_mfma_f32_16x16x32_f16 v[90:93], v[228:231], v[180:183], v[90:93]
	v_mfma_f32_16x16x32_f16 v[94:97], v[228:231], v[188:191], v[94:97]
	s_barrier
	s_mov_b32 m0, s86
	v_lshl_add_u64 v[176:177], v[250:251], 0, s[42:43]
	global_load_lds_dwordx4 v[176:177], off
	s_mov_b32 m0, s87
	v_lshl_add_u64 v[176:177], v[252:253], 0, s[42:43]
	global_load_lds_dwordx4 v[176:177], off
	s_waitcnt vmcnt(6)
	s_barrier
	v_mfma_f32_16x16x32_f16 v[98:101], v[196:199], v[232:235], v[98:101]
	v_mfma_f32_16x16x32_f16 v[102:105], v[196:199], v[240:243], v[102:105]
	v_mfma_f32_16x16x32_f16 v[106:109], v[204:207], v[232:235], v[106:109]
	v_mfma_f32_16x16x32_f16 v[110:113], v[204:207], v[240:243], v[110:113]
	v_mfma_f32_16x16x32_f16 v[114:117], v[216:219], v[232:235], v[114:117]
	v_mfma_f32_16x16x32_f16 v[118:121], v[216:219], v[240:243], v[118:121]
	v_mfma_f32_16x16x32_f16 v[122:125], v[224:227], v[232:235], v[122:125]
	v_mfma_f32_16x16x32_f16 v[126:129], v[224:227], v[240:243], v[126:129]
	v_mfma_f32_16x16x32_f16 v[98:101], v[200:203], v[236:239], v[98:101]
	v_mfma_f32_16x16x32_f16 v[102:105], v[200:203], v[244:247], v[102:105]
	v_mfma_f32_16x16x32_f16 v[106:109], v[212:215], v[236:239], v[106:109]
	v_mfma_f32_16x16x32_f16 v[110:113], v[212:215], v[244:247], v[110:113]
	v_mfma_f32_16x16x32_f16 v[114:117], v[220:223], v[236:239], v[114:117]
	v_mfma_f32_16x16x32_f16 v[118:121], v[220:223], v[244:247], v[118:121]
	v_mfma_f32_16x16x32_f16 v[122:125], v[228:231], v[236:239], v[122:125]
	v_mfma_f32_16x16x32_f16 v[126:129], v[228:231], v[244:247], v[126:129]
	s_add_i32 s48, s48, 2
	s_add_u32 s46, s46, 0x100
	s_addc_u32 s47, s47, 0
	s_cmp_lt_u32 s48, 4
	s_barrier
	s_cbranch_scc1 .LBB7_239
	s_add_u32 s0, s0, 0x20380
	s_addc_u32 s1, s1, 0
	v_readfirstlane_b32 s5, v174
	v_lshl_add_u64 v[130:131], v[130:131], 1, s[0:1]
	s_mov_b32 m0, s5
	ds_read_b128 v[134:137], v169
	ds_read_b128 v[138:141], v170
	ds_read_b128 v[152:155], v171
	ds_read_b128 v[156:159], v172
	ds_read_b128 v[166:169], v173
	ds_read_b128 v[176:179], v173 offset:1024
	ds_read_b128 v[180:183], v173 offset:2048
	ds_read_b128 v[184:187], v173 offset:3072
	ds_read_b128 v[188:191], v173 offset:4096
	ds_read_b128 v[196:199], v173 offset:5120
	ds_read_b128 v[200:203], v173 offset:6144
	ds_read_b128 v[204:207], v173 offset:7168
	global_load_lds_dwordx4 v[130:131], off
	v_lshl_add_u64 v[130:131], v[132:133], 1, s[0:1]
	v_readfirstlane_b32 s0, v175
	s_mov_b32 m0, s0
	s_nop 0
	global_load_lds_dwordx4 v[130:131], off
	s_barrier
	s_waitcnt lgkmcnt(0)
	v_mfma_f32_16x16x32_f16 v[2:5], v[166:169], v[134:137], v[2:5]
	v_mfma_f32_16x16x32_f16 v[42:45], v[188:191], v[152:155], v[42:45]
	v_mfma_f32_16x16x32_f16 v[54:57], v[200:203], v[134:137], v[54:57]
	v_mfma_f32_16x16x32_f16 v[66:69], v[200:203], v[152:155], v[66:69]
	v_mfma_f32_16x16x32_f16 v[2:5], v[176:179], v[138:141], v[2:5]
	v_mfma_f32_16x16x32_f16 v[6:9], v[166:169], v[152:155], v[6:9]
	v_mfma_f32_16x16x32_f16 v[10:13], v[180:183], v[134:137], v[10:13]
	v_mfma_f32_16x16x32_f16 v[18:21], v[180:183], v[152:155], v[18:21]
	v_mfma_f32_16x16x32_f16 v[30:33], v[188:191], v[134:137], v[30:33]
	v_mfma_f32_16x16x32_f16 v[42:45], v[196:199], v[156:159], v[42:45]
	v_mfma_f32_16x16x32_f16 v[54:57], v[204:207], v[138:141], v[54:57]
	v_mfma_f32_16x16x32_f16 v[66:69], v[204:207], v[156:159], v[66:69]
	v_mfma_f32_16x16x32_f16 v[6:9], v[176:179], v[156:159], v[6:9]
	v_mfma_f32_16x16x32_f16 v[10:13], v[184:187], v[138:141], v[10:13]
	v_mfma_f32_16x16x32_f16 v[18:21], v[184:187], v[156:159], v[18:21]
	v_mfma_f32_16x16x32_f16 v[30:33], v[196:199], v[138:141], v[30:33]
	s_barrier
	ds_read_b128 v[130:133], v161
	ds_read_b128 v[212:215], v162
	ds_read_b128 v[160:163], v163
	ds_read_b128 v[216:219], v164
	s_barrier
	s_waitcnt lgkmcnt(0)
	v_mfma_f32_16x16x32_f16 v[14:17], v[166:169], v[130:133], v[14:17]
	v_mfma_f32_16x16x32_f16 v[78:81], v[200:203], v[130:133], v[78:81]
	v_mfma_f32_16x16x32_f16 v[14:17], v[176:179], v[212:215], v[14:17]
	v_mfma_f32_16x16x32_f16 v[22:25], v[166:169], v[160:163], v[22:25]
	v_mfma_f32_16x16x32_f16 v[34:37], v[180:183], v[130:133], v[34:37]
	v_mfma_f32_16x16x32_f16 v[46:49], v[180:183], v[160:163], v[46:49]
	v_mfma_f32_16x16x32_f16 v[58:61], v[188:191], v[130:133], v[58:61]
	v_mfma_f32_16x16x32_f16 v[70:73], v[188:191], v[160:163], v[70:73]
	v_mfma_f32_16x16x32_f16 v[164:167], v[204:207], v[212:215], v[78:81]
	v_mfma_f32_16x16x32_f16 v[78:81], v[200:203], v[160:163], v[86:89]
	v_mfma_f32_16x16x32_f16 v[22:25], v[176:179], v[216:219], v[22:25]
	v_mfma_f32_16x16x32_f16 v[34:37], v[184:187], v[212:215], v[34:37]
	v_mfma_f32_16x16x32_f16 v[46:49], v[184:187], v[216:219], v[46:49]
	v_mfma_f32_16x16x32_f16 v[58:61], v[196:199], v[212:215], v[58:61]
	v_mfma_f32_16x16x32_f16 v[70:73], v[196:199], v[216:219], v[70:73]
	v_mfma_f32_16x16x32_f16 v[86:89], v[204:207], v[216:219], v[78:81]
	s_barrier
	s_nop 0
	ds_read_b128 v[78:81], v173 offset:16384
	ds_read_b128 v[168:171], v173 offset:17408
	ds_read_b128 v[174:177], v173 offset:18432
	ds_read_b128 v[178:181], v173 offset:19456
	ds_read_b128 v[182:185], v173 offset:20480
	ds_read_b128 v[186:189], v173 offset:21504
	ds_read_b128 v[190:193], v173 offset:22528
	ds_read_b128 v[196:199], v173 offset:23552
	s_waitcnt vmcnt(4)
	s_barrier
	s_waitcnt lgkmcnt(0)
	v_mfma_f32_16x16x32_f16 v[26:29], v[78:81], v[134:137], v[26:29]
	v_mfma_f32_16x16x32_f16 v[38:41], v[78:81], v[152:155], v[38:41]
	v_mfma_f32_16x16x32_f16 v[26:29], v[168:171], v[138:141], v[26:29]
	v_mfma_f32_16x16x32_f16 v[38:41], v[168:171], v[156:159], v[38:41]
	v_mfma_f32_16x16x32_f16 v[50:53], v[174:177], v[134:137], v[50:53]
	v_mfma_f32_16x16x32_f16 v[62:65], v[174:177], v[152:155], v[62:65]
	v_mfma_f32_16x16x32_f16 v[74:77], v[182:185], v[134:137], v[74:77]
	v_mfma_f32_16x16x32_f16 v[82:85], v[182:185], v[152:155], v[82:85]
	v_mfma_f32_16x16x32_f16 v[90:93], v[190:193], v[134:137], v[90:93]
	v_mfma_f32_16x16x32_f16 v[94:97], v[190:193], v[152:155], v[94:97]
	v_mfma_f32_16x16x32_f16 v[50:53], v[178:181], v[138:141], v[50:53]
	v_mfma_f32_16x16x32_f16 v[62:65], v[178:181], v[156:159], v[62:65]
	v_mfma_f32_16x16x32_f16 v[74:77], v[186:189], v[138:141], v[74:77]
	v_mfma_f32_16x16x32_f16 v[82:85], v[186:189], v[156:159], v[82:85]
	v_mfma_f32_16x16x32_f16 v[90:93], v[196:199], v[138:141], v[90:93]
	v_mfma_f32_16x16x32_f16 v[94:97], v[196:199], v[156:159], v[94:97]
	v_mfma_f32_16x16x32_f16 v[98:101], v[78:81], v[130:133], v[98:101]
	v_mfma_f32_16x16x32_f16 v[78:81], v[78:81], v[160:163], v[102:105]
	v_mfma_f32_16x16x32_f16 v[102:105], v[168:171], v[216:219], v[78:81]
	v_mfma_f32_16x16x32_f16 v[78:81], v[174:177], v[130:133], v[106:109]
	v_mfma_f32_16x16x32_f16 v[106:109], v[178:181], v[212:215], v[78:81]
	v_mfma_f32_16x16x32_f16 v[78:81], v[174:177], v[160:163], v[110:113]
	v_mfma_f32_16x16x32_f16 v[200:203], v[178:181], v[216:219], v[78:81]
	v_mfma_f32_16x16x32_f16 v[78:81], v[182:185], v[130:133], v[114:117]
	v_mfma_f32_16x16x32_f16 v[204:207], v[186:189], v[212:215], v[78:81]
	v_mfma_f32_16x16x32_f16 v[78:81], v[182:185], v[160:163], v[118:121]
	v_mfma_f32_16x16x32_f16 v[220:223], v[186:189], v[216:219], v[78:81]
	v_mfma_f32_16x16x32_f16 v[78:81], v[190:193], v[130:133], v[122:125]
	v_mfma_f32_16x16x32_f16 v[98:101], v[168:171], v[212:215], v[98:101]
	v_mfma_f32_16x16x32_f16 v[212:215], v[196:199], v[212:215], v[78:81]
	v_mfma_f32_16x16x32_f16 v[78:81], v[190:193], v[160:163], v[126:129]
	v_mfma_f32_16x16x32_f16 v[196:199], v[196:199], v[216:219], v[78:81]
	s_barrier
	ds_read_b128 v[110:113], v148
	ds_read_b128 v[130:133], v149
	ds_read_b128 v[216:219], v150
	ds_read_b128 v[224:227], v151
	s_nop 0
	ds_read_b128 v[78:81], v173 offset:32768
	ds_read_b128 v[114:117], v173 offset:33792
	ds_read_b128 v[118:121], v173 offset:34816
	ds_read_b128 v[134:137], v173 offset:35840
	ds_read_b128 v[138:141], v173 offset:36864
	ds_read_b128 v[168:171], v173 offset:37888
	ds_read_b128 v[174:177], v173 offset:38912
	ds_read_b128 v[228:231], v173 offset:39936
	s_waitcnt vmcnt(2)
	s_barrier
	s_waitcnt lgkmcnt(0)
	v_mfma_f32_16x16x32_f16 v[2:5], v[78:81], v[110:113], v[2:5]
	v_mfma_f32_16x16x32_f16 v[190:193], v[114:117], v[130:133], v[2:5]
	v_mfma_f32_16x16x32_f16 v[2:5], v[78:81], v[216:219], v[6:9]
	v_mfma_f32_16x16x32_f16 v[158:161], v[114:117], v[224:227], v[2:5]
	v_mfma_f32_16x16x32_f16 v[2:5], v[118:121], v[110:113], v[10:13]
	v_mfma_f32_16x16x32_f16 v[186:189], v[134:137], v[130:133], v[2:5]
	v_mfma_f32_16x16x32_f16 v[2:5], v[118:121], v[216:219], v[18:21]
	v_mfma_f32_16x16x32_f16 v[154:157], v[134:137], v[224:227], v[2:5]
	v_mfma_f32_16x16x32_f16 v[2:5], v[138:141], v[110:113], v[30:33]
	v_mfma_f32_16x16x32_f16 v[182:185], v[168:171], v[130:133], v[2:5]
	v_mfma_f32_16x16x32_f16 v[2:5], v[138:141], v[216:219], v[42:45]
	v_mfma_f32_16x16x32_f16 v[150:153], v[168:171], v[224:227], v[2:5]
	v_mfma_f32_16x16x32_f16 v[2:5], v[174:177], v[110:113], v[54:57]
	v_mfma_f32_16x16x32_f16 v[178:181], v[228:231], v[130:133], v[2:5]
	v_mfma_f32_16x16x32_f16 v[2:5], v[174:177], v[216:219], v[66:69]
	v_mfma_f32_16x16x32_f16 v[146:149], v[228:231], v[224:227], v[2:5]
	s_barrier
	s_nop 4
	ds_read_b128 v[2:5], v142
	ds_read_b128 v[6:9], v143
	ds_read_b128 v[10:13], v144
	ds_read_b128 v[18:21], v145
	s_waitcnt vmcnt(0)
	s_barrier
	s_waitcnt lgkmcnt(0)
	v_mfma_f32_16x16x32_f16 v[14:17], v[78:81], v[2:5], v[14:17]
	v_mfma_f32_16x16x32_f16 v[126:129], v[114:117], v[6:9], v[14:17]
	v_mfma_f32_16x16x32_f16 v[14:17], v[78:81], v[10:13], v[22:25]
	v_mfma_f32_16x16x32_f16 v[78:81], v[114:117], v[18:21], v[14:17]
	v_mfma_f32_16x16x32_f16 v[14:17], v[118:121], v[2:5], v[34:37]
	v_mfma_f32_16x16x32_f16 v[122:125], v[134:137], v[6:9], v[14:17]
	v_mfma_f32_16x16x32_f16 v[14:17], v[118:121], v[10:13], v[46:49]
	v_mfma_f32_16x16x32_f16 v[66:69], v[134:137], v[18:21], v[14:17]
	v_mfma_f32_16x16x32_f16 v[14:17], v[138:141], v[2:5], v[58:61]
	v_mfma_f32_16x16x32_f16 v[118:121], v[168:171], v[6:9], v[14:17]
	v_mfma_f32_16x16x32_f16 v[14:17], v[138:141], v[10:13], v[70:73]
	v_mfma_f32_16x16x32_f16 v[54:57], v[168:171], v[18:21], v[14:17]
	v_mfma_f32_16x16x32_f16 v[14:17], v[174:177], v[2:5], v[164:167]
	v_mfma_f32_16x16x32_f16 v[114:117], v[228:231], v[6:9], v[14:17]
	v_mfma_f32_16x16x32_f16 v[14:17], v[174:177], v[10:13], v[86:89]
	v_mfma_f32_16x16x32_f16 v[42:45], v[228:231], v[18:21], v[14:17]
	s_barrier
	s_nop 4
	ds_read_b128 v[14:17], v173 offset:49152
	ds_read_b128 v[22:25], v173 offset:50176
	ds_read_b128 v[30:33], v173 offset:51200
	ds_read_b128 v[34:37], v173 offset:52224
	ds_read_b128 v[46:49], v173 offset:53248
	ds_read_b128 v[58:61], v173 offset:54272
	ds_read_b128 v[70:73], v173 offset:55296
	ds_read_b128 v[86:89], v173 offset:56320
	s_barrier
	s_waitcnt lgkmcnt(0)
	v_mfma_f32_16x16x32_f16 v[26:29], v[14:17], v[110:113], v[26:29]
	v_mfma_f32_16x16x32_f16 v[174:177], v[22:25], v[130:133], v[26:29]
	v_mfma_f32_16x16x32_f16 v[26:29], v[14:17], v[216:219], v[38:41]
	v_mfma_f32_16x16x32_f16 v[142:145], v[22:25], v[224:227], v[26:29]
	v_mfma_f32_16x16x32_f16 v[26:29], v[30:33], v[110:113], v[50:53]
	v_mfma_f32_16x16x32_f16 v[170:173], v[34:37], v[130:133], v[26:29]
	v_mfma_f32_16x16x32_f16 v[26:29], v[30:33], v[216:219], v[62:65]
	v_mfma_f32_16x16x32_f16 v[138:141], v[34:37], v[224:227], v[26:29]
	v_mfma_f32_16x16x32_f16 v[26:29], v[46:49], v[110:113], v[74:77]
	v_mfma_f32_16x16x32_f16 v[166:169], v[58:61], v[130:133], v[26:29]
	v_mfma_f32_16x16x32_f16 v[26:29], v[46:49], v[216:219], v[82:85]
	v_mfma_f32_16x16x32_f16 v[134:137], v[58:61], v[224:227], v[26:29]
	v_mfma_f32_16x16x32_f16 v[26:29], v[70:73], v[110:113], v[90:93]
	v_mfma_f32_16x16x32_f16 v[162:165], v[86:89], v[130:133], v[26:29]
	v_mfma_f32_16x16x32_f16 v[26:29], v[70:73], v[216:219], v[94:97]
	v_mfma_f32_16x16x32_f16 v[130:133], v[86:89], v[224:227], v[26:29]
	v_mfma_f32_16x16x32_f16 v[26:29], v[14:17], v[2:5], v[98:101]
	v_mfma_f32_16x16x32_f16 v[14:17], v[14:17], v[10:13], v[102:105]
	v_mfma_f32_16x16x32_f16 v[38:41], v[22:25], v[18:21], v[14:17]
	v_mfma_f32_16x16x32_f16 v[14:17], v[30:33], v[2:5], v[106:109]
	v_mfma_f32_16x16x32_f16 v[106:109], v[34:37], v[6:9], v[14:17]
	v_mfma_f32_16x16x32_f16 v[14:17], v[30:33], v[10:13], v[200:203]
	v_mfma_f32_16x16x32_f16 v[110:113], v[22:25], v[6:9], v[26:29]
	v_mfma_f32_16x16x32_f16 v[26:29], v[34:37], v[18:21], v[14:17]
	v_mfma_f32_16x16x32_f16 v[14:17], v[46:49], v[2:5], v[204:207]
	v_mfma_f32_16x16x32_f16 v[2:5], v[70:73], v[2:5], v[212:215]
	v_mfma_f32_16x16x32_f16 v[102:105], v[58:61], v[6:9], v[14:17]
	v_mfma_f32_16x16x32_f16 v[14:17], v[46:49], v[10:13], v[220:223]
	v_mfma_f32_16x16x32_f16 v[98:101], v[86:89], v[6:9], v[2:5]
	v_mfma_f32_16x16x32_f16 v[2:5], v[70:73], v[10:13], v[196:199]
	v_mfma_f32_16x16x32_f16 v[14:17], v[58:61], v[18:21], v[14:17]
	v_mfma_f32_16x16x32_f16 v[2:5], v[86:89], v[18:21], v[2:5]
	s_cmpk_gt_u32 s65, 0xff
	s_barrier
	s_cbranch_scc1 .LBB7_242
	s_barrier

.LBB8_41:
	ds_read_b128 v[182:185], v171
	ds_read_b128 v[190:193], v174
	ds_read_b128 v[186:189], v173
	ds_read_b128 v[194:197], v175
	v_add_u32_e32 v177, 0xc000, v148
	v_lshl_add_u64 v[246:247], v[134:135], 0, s[44:45]
	v_add_u32_e32 v176, s48, v170
	v_lshl_add_u64 v[178:179], v[246:247], 0, s[28:29]
	s_mov_b32 m0, s75
	ds_read_b128 v[198:201], v176
	ds_read_b128 v[206:209], v176 offset:2048
	ds_read_b128 v[214:217], v176 offset:4096
	ds_read_b128 v[222:225], v176 offset:6144
	ds_read_b128 v[202:205], v176 offset:1024
	ds_read_b128 v[210:213], v176 offset:3072
	ds_read_b128 v[218:221], v176 offset:5120
	ds_read_b128 v[226:229], v176 offset:7168
	global_load_lds_dwordx4 v[178:179], off
	v_add_u32_e32 v178, 0xe000, v148
	v_lshl_add_u64 v[248:249], v[136:137], 0, s[44:45]
	s_mov_b32 m0, s76
	v_lshl_add_u64 v[230:231], v[248:249], 0, s[28:29]
	global_load_lds_dwordx4 v[230:231], off
	s_waitcnt lgkmcnt(8)
	s_barrier
	s_waitcnt lgkmcnt(4)
	v_mfma_f32_16x16x32_f16 v[126:129], v[198:201], v[182:185], v[126:129]
	v_mfma_f32_16x16x32_f16 v[122:125], v[198:201], v[190:193], v[122:125]
	v_mfma_f32_16x16x32_f16 v[118:121], v[206:209], v[182:185], v[118:121]
	v_mfma_f32_16x16x32_f16 v[114:117], v[206:209], v[190:193], v[114:117]
	v_mfma_f32_16x16x32_f16 v[110:113], v[214:217], v[182:185], v[110:113]
	v_mfma_f32_16x16x32_f16 v[106:109], v[214:217], v[190:193], v[106:109]
	v_mfma_f32_16x16x32_f16 v[102:105], v[222:225], v[182:185], v[102:105]
	v_mfma_f32_16x16x32_f16 v[98:101], v[222:225], v[190:193], v[98:101]
	s_waitcnt lgkmcnt(0)
	v_mfma_f32_16x16x32_f16 v[126:129], v[202:205], v[186:189], v[126:129]
	v_mfma_f32_16x16x32_f16 v[122:125], v[202:205], v[194:197], v[122:125]
	v_mfma_f32_16x16x32_f16 v[118:121], v[210:213], v[186:189], v[118:121]
	v_mfma_f32_16x16x32_f16 v[114:117], v[210:213], v[194:197], v[114:117]
	v_mfma_f32_16x16x32_f16 v[110:113], v[218:221], v[186:189], v[110:113]
	v_mfma_f32_16x16x32_f16 v[106:109], v[218:221], v[194:197], v[106:109]
	v_mfma_f32_16x16x32_f16 v[102:105], v[226:229], v[186:189], v[102:105]
	v_mfma_f32_16x16x32_f16 v[98:101], v[226:229], v[194:197], v[98:101]
	s_barrier
	v_lshl_add_u64 v[250:251], v[138:139], 0, s[44:45]
	v_lshl_add_u64 v[252:253], v[250:251], 0, s[30:31]
	s_mov_b32 m0, s77
	ds_read_b128 v[230:233], v162
	ds_read_b128 v[238:241], v164
	ds_read_b128 v[234:237], v163
	ds_read_b128 v[242:245], v165
	global_load_lds_dwordx4 v[252:253], off
	v_lshl_add_u64 v[252:253], v[140:141], 0, s[44:45]
	s_mov_b32 m0, s78
	v_lshl_add_u64 v[254:255], v[252:253], 0, s[30:31]
	global_load_lds_dwordx4 v[254:255], off
	s_barrier
	s_waitcnt lgkmcnt(2)
	v_mfma_f32_16x16x32_f16 v[94:97], v[198:201], v[230:233], v[94:97]
	v_mfma_f32_16x16x32_f16 v[90:93], v[198:201], v[238:241], v[90:93]
	v_mfma_f32_16x16x32_f16 v[86:89], v[206:209], v[230:233], v[86:89]
	v_mfma_f32_16x16x32_f16 v[82:85], v[206:209], v[238:241], v[82:85]
	v_mfma_f32_16x16x32_f16 v[78:81], v[214:217], v[230:233], v[78:81]
	v_mfma_f32_16x16x32_f16 v[74:77], v[214:217], v[238:241], v[74:77]
	v_mfma_f32_16x16x32_f16 v[70:73], v[222:225], v[230:233], v[70:73]
	v_mfma_f32_16x16x32_f16 v[66:69], v[222:225], v[238:241], v[66:69]
	s_waitcnt lgkmcnt(0)
	v_mfma_f32_16x16x32_f16 v[94:97], v[202:205], v[234:237], v[94:97]
	v_mfma_f32_16x16x32_f16 v[90:93], v[202:205], v[242:245], v[90:93]
	v_mfma_f32_16x16x32_f16 v[86:89], v[210:213], v[234:237], v[86:89]
	v_mfma_f32_16x16x32_f16 v[82:85], v[210:213], v[242:245], v[82:85]
	v_mfma_f32_16x16x32_f16 v[78:81], v[218:221], v[234:237], v[78:81]
	v_mfma_f32_16x16x32_f16 v[74:77], v[218:221], v[242:245], v[74:77]
	v_mfma_f32_16x16x32_f16 v[70:73], v[226:229], v[234:237], v[70:73]
	v_mfma_f32_16x16x32_f16 v[66:69], v[226:229], v[242:245], v[66:69]
	v_lshl_add_u64 v[254:255], v[246:247], 0, s[30:31]
	s_mov_b32 m0, s79
	s_barrier
	ds_read_b128 v[198:201], v176 offset:16384
	ds_read_b128 v[206:209], v176 offset:18432
	ds_read_b128 v[214:217], v176 offset:20480
	ds_read_b128 v[222:225], v176 offset:22528
	ds_read_b128 v[202:205], v176 offset:17408
	ds_read_b128 v[210:213], v176 offset:19456
	ds_read_b128 v[218:221], v176 offset:21504
	ds_read_b128 v[226:229], v176 offset:23552
	global_load_lds_dwordx4 v[254:255], off
	s_mov_b32 m0, s80
	v_lshl_add_u64 v[254:255], v[248:249], 0, s[30:31]
	global_load_lds_dwordx4 v[254:255], off
	s_barrier
	s_waitcnt lgkmcnt(4)
	v_mfma_f32_16x16x32_f16 v[62:65], v[198:201], v[182:185], v[62:65]
	v_mfma_f32_16x16x32_f16 v[58:61], v[198:201], v[190:193], v[58:61]
	v_mfma_f32_16x16x32_f16 v[54:57], v[206:209], v[182:185], v[54:57]
	v_mfma_f32_16x16x32_f16 v[50:53], v[206:209], v[190:193], v[50:53]
	v_mfma_f32_16x16x32_f16 v[46:49], v[214:217], v[182:185], v[46:49]
	v_mfma_f32_16x16x32_f16 v[42:45], v[214:217], v[190:193], v[42:45]
	v_mfma_f32_16x16x32_f16 v[38:41], v[222:225], v[182:185], v[38:41]
	v_mfma_f32_16x16x32_f16 v[34:37], v[222:225], v[190:193], v[34:37]
	s_waitcnt lgkmcnt(0)
	v_mfma_f32_16x16x32_f16 v[62:65], v[202:205], v[186:189], v[62:65]
	v_mfma_f32_16x16x32_f16 v[58:61], v[202:205], v[194:197], v[58:61]
	v_mfma_f32_16x16x32_f16 v[54:57], v[210:213], v[186:189], v[54:57]
	v_mfma_f32_16x16x32_f16 v[50:53], v[210:213], v[194:197], v[50:53]
	v_mfma_f32_16x16x32_f16 v[46:49], v[218:221], v[186:189], v[46:49]
	v_mfma_f32_16x16x32_f16 v[42:45], v[218:221], v[194:197], v[42:45]
	v_mfma_f32_16x16x32_f16 v[38:41], v[226:229], v[186:189], v[38:41]
	v_mfma_f32_16x16x32_f16 v[34:37], v[226:229], v[194:197], v[34:37]
	s_barrier
	s_mov_b32 m0, s81
	v_lshl_add_u64 v[182:183], v[250:251], 0, s[34:35]
	global_load_lds_dwordx4 v[182:183], off
	s_mov_b32 m0, s82
	v_lshl_add_u64 v[182:183], v[252:253], 0, s[34:35]
	global_load_lds_dwordx4 v[182:183], off
	s_waitcnt vmcnt(6)
	s_barrier
	v_mfma_f32_16x16x32_f16 v[30:33], v[198:201], v[230:233], v[30:33]
	v_mfma_f32_16x16x32_f16 v[26:29], v[198:201], v[238:241], v[26:29]
	v_mfma_f32_16x16x32_f16 v[22:25], v[206:209], v[230:233], v[22:25]
	v_mfma_f32_16x16x32_f16 v[18:21], v[206:209], v[238:241], v[18:21]
	v_mfma_f32_16x16x32_f16 v[14:17], v[214:217], v[230:233], v[14:17]
	v_mfma_f32_16x16x32_f16 v[10:13], v[214:217], v[238:241], v[10:13]
	v_mfma_f32_16x16x32_f16 v[6:9], v[222:225], v[230:233], v[6:9]
	v_mfma_f32_16x16x32_f16 v[2:5], v[222:225], v[238:241], v[2:5]
	v_mfma_f32_16x16x32_f16 v[30:33], v[202:205], v[234:237], v[30:33]
	v_mfma_f32_16x16x32_f16 v[26:29], v[202:205], v[242:245], v[26:29]
	v_mfma_f32_16x16x32_f16 v[22:25], v[210:213], v[234:237], v[22:25]
	v_mfma_f32_16x16x32_f16 v[18:21], v[210:213], v[242:245], v[18:21]
	v_mfma_f32_16x16x32_f16 v[14:17], v[218:221], v[234:237], v[14:17]
	v_mfma_f32_16x16x32_f16 v[10:13], v[218:221], v[242:245], v[10:13]
	v_mfma_f32_16x16x32_f16 v[6:9], v[226:229], v[234:237], v[6:9]
	v_mfma_f32_16x16x32_f16 v[2:5], v[226:229], v[242:245], v[2:5]
	s_barrier
	ds_read_b128 v[182:185], v144
	ds_read_b128 v[190:193], v146
	ds_read_b128 v[186:189], v145
	ds_read_b128 v[194:197], v147
	v_lshl_add_u64 v[230:231], v[246:247], 0, s[34:35]
	s_mov_b32 m0, s83
	ds_read_b128 v[198:201], v176 offset:32768
	ds_read_b128 v[206:209], v176 offset:34816
	ds_read_b128 v[214:217], v176 offset:36864
	ds_read_b128 v[222:225], v176 offset:38912
	ds_read_b128 v[202:205], v176 offset:33792
	ds_read_b128 v[210:213], v176 offset:35840
	ds_read_b128 v[218:221], v176 offset:37888
	ds_read_b128 v[226:229], v176 offset:39936
	global_load_lds_dwordx4 v[230:231], off
	s_mov_b32 m0, s84
	v_lshl_add_u64 v[230:231], v[248:249], 0, s[34:35]
	global_load_lds_dwordx4 v[230:231], off
	s_waitcnt lgkmcnt(8)
	s_barrier
	s_waitcnt lgkmcnt(4)
	v_mfma_f32_16x16x32_f16 v[126:129], v[198:201], v[182:185], v[126:129]
	v_mfma_f32_16x16x32_f16 v[122:125], v[198:201], v[190:193], v[122:125]
	v_mfma_f32_16x16x32_f16 v[118:121], v[206:209], v[182:185], v[118:121]
	v_mfma_f32_16x16x32_f16 v[114:117], v[206:209], v[190:193], v[114:117]
	v_mfma_f32_16x16x32_f16 v[110:113], v[214:217], v[182:185], v[110:113]
	v_mfma_f32_16x16x32_f16 v[106:109], v[214:217], v[190:193], v[106:109]
	v_mfma_f32_16x16x32_f16 v[102:105], v[222:225], v[182:185], v[102:105]
	v_mfma_f32_16x16x32_f16 v[98:101], v[222:225], v[190:193], v[98:101]
	s_waitcnt lgkmcnt(0)
	v_mfma_f32_16x16x32_f16 v[126:129], v[202:205], v[186:189], v[126:129]
	v_mfma_f32_16x16x32_f16 v[122:125], v[202:205], v[194:197], v[122:125]
	v_mfma_f32_16x16x32_f16 v[118:121], v[210:213], v[186:189], v[118:121]
	v_mfma_f32_16x16x32_f16 v[114:117], v[210:213], v[194:197], v[114:117]
	v_mfma_f32_16x16x32_f16 v[110:113], v[218:221], v[186:189], v[110:113]
	v_mfma_f32_16x16x32_f16 v[106:109], v[218:221], v[194:197], v[106:109]
	v_mfma_f32_16x16x32_f16 v[102:105], v[226:229], v[186:189], v[102:105]
	v_mfma_f32_16x16x32_f16 v[98:101], v[226:229], v[194:197], v[98:101]
	s_barrier
	v_lshl_add_u64 v[254:255], v[250:251], 0, s[36:37]
	s_mov_b32 m0, s85
	ds_read_b128 v[230:233], v150
	ds_read_b128 v[238:241], v152
	ds_read_b128 v[234:237], v151
	ds_read_b128 v[242:245], v153
	global_load_lds_dwordx4 v[254:255], off
	s_mov_b32 m0, s86
	v_lshl_add_u64 v[254:255], v[252:253], 0, s[36:37]
	global_load_lds_dwordx4 v[254:255], off
	s_barrier
	s_waitcnt lgkmcnt(2)
	v_mfma_f32_16x16x32_f16 v[94:97], v[198:201], v[230:233], v[94:97]
	v_mfma_f32_16x16x32_f16 v[90:93], v[198:201], v[238:241], v[90:93]
	v_mfma_f32_16x16x32_f16 v[86:89], v[206:209], v[230:233], v[86:89]
	v_mfma_f32_16x16x32_f16 v[82:85], v[206:209], v[238:241], v[82:85]
	v_mfma_f32_16x16x32_f16 v[78:81], v[214:217], v[230:233], v[78:81]
	v_mfma_f32_16x16x32_f16 v[74:77], v[214:217], v[238:241], v[74:77]
	v_mfma_f32_16x16x32_f16 v[70:73], v[222:225], v[230:233], v[70:73]
	v_mfma_f32_16x16x32_f16 v[66:69], v[222:225], v[238:241], v[66:69]
	s_waitcnt lgkmcnt(0)
	v_mfma_f32_16x16x32_f16 v[94:97], v[202:205], v[234:237], v[94:97]
	v_mfma_f32_16x16x32_f16 v[90:93], v[202:205], v[242:245], v[90:93]
	v_mfma_f32_16x16x32_f16 v[86:89], v[210:213], v[234:237], v[86:89]
	v_mfma_f32_16x16x32_f16 v[82:85], v[210:213], v[242:245], v[82:85]
	v_mfma_f32_16x16x32_f16 v[78:81], v[218:221], v[234:237], v[78:81]
	v_mfma_f32_16x16x32_f16 v[74:77], v[218:221], v[242:245], v[74:77]
	v_mfma_f32_16x16x32_f16 v[70:73], v[226:229], v[234:237], v[70:73]
	v_mfma_f32_16x16x32_f16 v[66:69], v[226:229], v[242:245], v[66:69]
	v_lshl_add_u64 v[246:247], v[246:247], 0, s[36:37]
	s_mov_b32 m0, s87
	s_barrier
	ds_read_b128 v[198:201], v176 offset:49152
	ds_read_b128 v[206:209], v176 offset:51200
	ds_read_b128 v[214:217], v176 offset:53248
	ds_read_b128 v[222:225], v176 offset:55296
	ds_read_b128 v[202:205], v176 offset:50176
	ds_read_b128 v[210:213], v176 offset:52224
	ds_read_b128 v[218:221], v176 offset:54272
	ds_read_b128 v[226:229], v176 offset:56320
	global_load_lds_dwordx4 v[246:247], off
	s_mov_b32 m0, s88
	v_lshl_add_u64 v[246:247], v[248:249], 0, s[36:37]
	global_load_lds_dwordx4 v[246:247], off
	s_barrier
	s_waitcnt lgkmcnt(4)
	v_mfma_f32_16x16x32_f16 v[62:65], v[198:201], v[182:185], v[62:65]
	v_mfma_f32_16x16x32_f16 v[58:61], v[198:201], v[190:193], v[58:61]
	v_mfma_f32_16x16x32_f16 v[54:57], v[206:209], v[182:185], v[54:57]
	v_mfma_f32_16x16x32_f16 v[50:53], v[206:209], v[190:193], v[50:53]
	v_mfma_f32_16x16x32_f16 v[46:49], v[214:217], v[182:185], v[46:49]
	v_mfma_f32_16x16x32_f16 v[42:45], v[214:217], v[190:193], v[42:45]
	v_mfma_f32_16x16x32_f16 v[38:41], v[222:225], v[182:185], v[38:41]
	v_mfma_f32_16x16x32_f16 v[34:37], v[222:225], v[190:193], v[34:37]
	s_waitcnt lgkmcnt(0)
	v_mfma_f32_16x16x32_f16 v[62:65], v[202:205], v[186:189], v[62:65]
	v_mfma_f32_16x16x32_f16 v[58:61], v[202:205], v[194:197], v[58:61]
	v_mfma_f32_16x16x32_f16 v[54:57], v[210:213], v[186:189], v[54:57]
	v_mfma_f32_16x16x32_f16 v[50:53], v[210:213], v[194:197], v[50:53]
	v_mfma_f32_16x16x32_f16 v[46:49], v[218:221], v[186:189], v[46:49]
	v_mfma_f32_16x16x32_f16 v[42:45], v[218:221], v[194:197], v[42:45]
	v_mfma_f32_16x16x32_f16 v[38:41], v[226:229], v[186:189], v[38:41]
	v_mfma_f32_16x16x32_f16 v[34:37], v[226:229], v[194:197], v[34:37]
	s_barrier
	s_mov_b32 m0, s89
	v_lshl_add_u64 v[182:183], v[250:251], 0, s[38:39]
	global_load_lds_dwordx4 v[182:183], off
	s_mov_b32 m0, s90
	v_lshl_add_u64 v[182:183], v[252:253], 0, s[38:39]
	global_load_lds_dwordx4 v[182:183], off
	s_waitcnt vmcnt(6)
	s_barrier
	v_mfma_f32_16x16x32_f16 v[30:33], v[198:201], v[230:233], v[30:33]
	v_mfma_f32_16x16x32_f16 v[26:29], v[198:201], v[238:241], v[26:29]
	v_mfma_f32_16x16x32_f16 v[22:25], v[206:209], v[230:233], v[22:25]
	v_mfma_f32_16x16x32_f16 v[18:21], v[206:209], v[238:241], v[18:21]
	v_mfma_f32_16x16x32_f16 v[14:17], v[214:217], v[230:233], v[14:17]
	v_mfma_f32_16x16x32_f16 v[10:13], v[214:217], v[238:241], v[10:13]
	v_mfma_f32_16x16x32_f16 v[6:9], v[222:225], v[230:233], v[6:9]
	v_mfma_f32_16x16x32_f16 v[2:5], v[222:225], v[238:241], v[2:5]
	v_mfma_f32_16x16x32_f16 v[30:33], v[202:205], v[234:237], v[30:33]
	v_mfma_f32_16x16x32_f16 v[26:29], v[202:205], v[242:245], v[26:29]
	v_mfma_f32_16x16x32_f16 v[22:25], v[210:213], v[234:237], v[22:25]
	v_mfma_f32_16x16x32_f16 v[18:21], v[210:213], v[242:245], v[18:21]
	v_mfma_f32_16x16x32_f16 v[14:17], v[218:221], v[234:237], v[14:17]
	v_mfma_f32_16x16x32_f16 v[10:13], v[218:221], v[242:245], v[10:13]
	v_mfma_f32_16x16x32_f16 v[6:9], v[226:229], v[234:237], v[6:9]
	v_mfma_f32_16x16x32_f16 v[2:5], v[226:229], v[242:245], v[2:5]
	s_add_i32 s46, s46, 2
	s_add_u32 s44, s44, 0x100
	s_addc_u32 s45, s45, 0
	s_cmp_lt_u32 s46, 4
	s_barrier
	s_cbranch_scc1 .LBB8_41
	s_add_u32 s42, s42, 0x20380
	s_addc_u32 s43, s43, 0
	v_readfirstlane_b32 s44, v177
	v_lshl_add_u64 v[130:131], v[130:131], 1, s[42:43]
	s_mov_b32 m0, s44
	ds_read_b128 v[134:137], v171
	ds_read_b128 v[138:141], v173
	ds_read_b128 v[154:157], v174
	ds_read_b128 v[168:171], v175
	ds_read_b128 v[182:185], v176
	ds_read_b128 v[186:189], v176 offset:1024
	ds_read_b128 v[190:193], v176 offset:2048
	ds_read_b128 v[194:197], v176 offset:3072
	ds_read_b128 v[198:201], v176 offset:4096
	ds_read_b128 v[202:205], v176 offset:5120
	ds_read_b128 v[206:209], v176 offset:6144
	ds_read_b128 v[210:213], v176 offset:7168
	global_load_lds_dwordx4 v[130:131], off
	v_lshl_add_u64 v[130:131], v[132:133], 1, s[42:43]
	v_readfirstlane_b32 s42, v178
	s_mov_b32 m0, s42
	s_nop 0
	global_load_lds_dwordx4 v[130:131], off
	s_barrier
	s_waitcnt lgkmcnt(0)
	v_mfma_f32_16x16x32_f16 v[122:125], v[182:185], v[154:157], v[122:125]
	v_mfma_f32_16x16x32_f16 v[110:113], v[198:201], v[134:137], v[110:113]
	v_mfma_f32_16x16x32_f16 v[98:101], v[206:209], v[154:157], v[98:101]
	v_mfma_f32_16x16x32_f16 v[126:129], v[182:185], v[134:137], v[126:129]
	v_mfma_f32_16x16x32_f16 v[122:125], v[186:189], v[168:171], v[122:125]
	v_mfma_f32_16x16x32_f16 v[118:121], v[190:193], v[134:137], v[118:121]
	v_mfma_f32_16x16x32_f16 v[114:117], v[190:193], v[154:157], v[114:117]
	v_mfma_f32_16x16x32_f16 v[130:133], v[202:205], v[138:141], v[110:113]
	v_mfma_f32_16x16x32_f16 v[106:109], v[198:201], v[154:157], v[106:109]
	v_mfma_f32_16x16x32_f16 v[102:105], v[206:209], v[134:137], v[102:105]
	v_mfma_f32_16x16x32_f16 v[98:101], v[210:213], v[168:171], v[98:101]
	v_mfma_f32_16x16x32_f16 v[126:129], v[186:189], v[138:141], v[126:129]
	v_mfma_f32_16x16x32_f16 v[118:121], v[194:197], v[138:141], v[118:121]
	v_mfma_f32_16x16x32_f16 v[114:117], v[194:197], v[168:171], v[114:117]
	v_mfma_f32_16x16x32_f16 v[214:217], v[202:205], v[168:171], v[106:109]
	v_mfma_f32_16x16x32_f16 v[102:105], v[210:213], v[138:141], v[102:105]
	s_barrier
	ds_read_b128 v[106:109], v162
	ds_read_b128 v[110:113], v163
	ds_read_b128 v[160:163], v164
	ds_read_b128 v[218:221], v165
	s_barrier
	s_waitcnt lgkmcnt(0)
	v_mfma_f32_16x16x32_f16 v[82:85], v[190:193], v[160:163], v[82:85]
	v_mfma_f32_16x16x32_f16 v[78:81], v[198:201], v[106:109], v[78:81]
	v_mfma_f32_16x16x32_f16 v[74:77], v[198:201], v[160:163], v[74:77]
	v_mfma_f32_16x16x32_f16 v[70:73], v[206:209], v[106:109], v[70:73]
	v_mfma_f32_16x16x32_f16 v[66:69], v[206:209], v[160:163], v[66:69]
	v_mfma_f32_16x16x32_f16 v[94:97], v[182:185], v[106:109], v[94:97]
	v_mfma_f32_16x16x32_f16 v[90:93], v[182:185], v[160:163], v[90:93]
	v_mfma_f32_16x16x32_f16 v[86:89], v[190:193], v[106:109], v[86:89]
	v_mfma_f32_16x16x32_f16 v[82:85], v[194:197], v[218:221], v[82:85]
	v_mfma_f32_16x16x32_f16 v[78:81], v[202:205], v[110:113], v[78:81]
	v_mfma_f32_16x16x32_f16 v[74:77], v[202:205], v[218:221], v[74:77]
	v_mfma_f32_16x16x32_f16 v[70:73], v[210:213], v[110:113], v[70:73]
	v_mfma_f32_16x16x32_f16 v[66:69], v[210:213], v[218:221], v[66:69]
	v_mfma_f32_16x16x32_f16 v[222:225], v[186:189], v[110:113], v[94:97]
	v_mfma_f32_16x16x32_f16 v[182:185], v[186:189], v[218:221], v[90:93]
	v_mfma_f32_16x16x32_f16 v[86:89], v[194:197], v[110:113], v[86:89]
	s_barrier
	ds_read_b128 v[90:93], v176 offset:16384
	ds_read_b128 v[94:97], v176 offset:17408
	ds_read_b128 v[186:189], v176 offset:18432
	ds_read_b128 v[190:193], v176 offset:19456
	ds_read_b128 v[194:197], v176 offset:20480
	ds_read_b128 v[198:201], v176 offset:21504
	ds_read_b128 v[202:205], v176 offset:22528
	ds_read_b128 v[206:209], v176 offset:23552
	s_waitcnt vmcnt(4)
	s_barrier
	s_waitcnt lgkmcnt(0)
	v_mfma_f32_16x16x32_f16 v[46:49], v[194:197], v[134:137], v[46:49]
	v_mfma_f32_16x16x32_f16 v[42:45], v[194:197], v[154:157], v[42:45]
	v_mfma_f32_16x16x32_f16 v[38:41], v[202:205], v[134:137], v[38:41]
	v_mfma_f32_16x16x32_f16 v[34:37], v[202:205], v[154:157], v[34:37]
	v_mfma_f32_16x16x32_f16 v[62:65], v[90:93], v[134:137], v[62:65]
	v_mfma_f32_16x16x32_f16 v[58:61], v[90:93], v[154:157], v[58:61]
	v_mfma_f32_16x16x32_f16 v[54:57], v[186:189], v[134:137], v[54:57]
	v_mfma_f32_16x16x32_f16 v[50:53], v[186:189], v[154:157], v[50:53]
	v_mfma_f32_16x16x32_f16 v[46:49], v[198:201], v[138:141], v[46:49]
	v_mfma_f32_16x16x32_f16 v[42:45], v[198:201], v[168:171], v[42:45]
	v_mfma_f32_16x16x32_f16 v[38:41], v[206:209], v[138:141], v[38:41]
	v_mfma_f32_16x16x32_f16 v[34:37], v[206:209], v[168:171], v[34:37]
	v_mfma_f32_16x16x32_f16 v[210:213], v[94:97], v[138:141], v[62:65]
	v_mfma_f32_16x16x32_f16 v[226:229], v[94:97], v[168:171], v[58:61]
	v_mfma_f32_16x16x32_f16 v[230:233], v[190:193], v[138:141], v[54:57]
	v_mfma_f32_16x16x32_f16 v[234:237], v[190:193], v[168:171], v[50:53]
	v_mfma_f32_16x16x32_f16 v[2:5], v[202:205], v[160:163], v[2:5]
	v_mfma_f32_16x16x32_f16 v[30:33], v[90:93], v[106:109], v[30:33]
	v_mfma_f32_16x16x32_f16 v[26:29], v[90:93], v[160:163], v[26:29]
	v_mfma_f32_16x16x32_f16 v[22:25], v[186:189], v[106:109], v[22:25]
	v_mfma_f32_16x16x32_f16 v[18:21], v[186:189], v[160:163], v[18:21]
	v_mfma_f32_16x16x32_f16 v[14:17], v[194:197], v[106:109], v[14:17]
	v_mfma_f32_16x16x32_f16 v[10:13], v[194:197], v[160:163], v[10:13]
	v_mfma_f32_16x16x32_f16 v[6:9], v[202:205], v[106:109], v[6:9]
	v_mfma_f32_16x16x32_f16 v[2:5], v[206:209], v[218:221], v[2:5]
	v_mfma_f32_16x16x32_f16 v[138:141], v[94:97], v[110:113], v[30:33]
	v_mfma_f32_16x16x32_f16 v[168:171], v[94:97], v[218:221], v[26:29]
	v_mfma_f32_16x16x32_f16 v[238:241], v[190:193], v[110:113], v[22:25]
	v_mfma_f32_16x16x32_f16 v[186:189], v[190:193], v[218:221], v[18:21]
	v_mfma_f32_16x16x32_f16 v[190:193], v[198:201], v[110:113], v[14:17]
	v_mfma_f32_16x16x32_f16 v[194:197], v[198:201], v[218:221], v[10:13]
	v_mfma_f32_16x16x32_f16 v[198:201], v[206:209], v[110:113], v[6:9]
	s_barrier
	s_nop 0
	ds_read_b128 v[6:9], v144
	ds_read_b128 v[10:13], v145
	ds_read_b128 v[14:17], v146
	ds_read_b128 v[160:163], v147
	ds_read_b128 v[18:21], v176 offset:32768
	ds_read_b128 v[22:25], v176 offset:33792
	ds_read_b128 v[26:29], v176 offset:34816
	ds_read_b128 v[50:53], v176 offset:35840
	ds_read_b128 v[202:205], v176 offset:36864
	ds_read_b128 v[206:209], v176 offset:37888
	ds_read_b128 v[218:221], v176 offset:38912
	ds_read_b128 v[242:245], v176 offset:39936
	s_waitcnt vmcnt(2)
	s_barrier
	s_waitcnt lgkmcnt(0)
	v_mfma_f32_16x16x32_f16 v[30:33], v[18:21], v[6:9], v[126:129]
	v_mfma_f32_16x16x32_f16 v[154:157], v[22:25], v[10:13], v[30:33]
	v_mfma_f32_16x16x32_f16 v[30:33], v[18:21], v[14:17], v[122:125]
	v_mfma_f32_16x16x32_f16 v[110:113], v[22:25], v[160:163], v[30:33]
	v_mfma_f32_16x16x32_f16 v[30:33], v[26:29], v[6:9], v[118:121]
	v_mfma_f32_16x16x32_f16 v[146:149], v[50:53], v[10:13], v[30:33]
	v_mfma_f32_16x16x32_f16 v[30:33], v[26:29], v[14:17], v[114:117]
	v_mfma_f32_16x16x32_f16 v[106:109], v[50:53], v[160:163], v[30:33]
	v_mfma_f32_16x16x32_f16 v[30:33], v[202:205], v[6:9], v[130:133]
	v_mfma_f32_16x16x32_f16 v[142:145], v[206:209], v[10:13], v[30:33]
	v_mfma_f32_16x16x32_f16 v[30:33], v[202:205], v[14:17], v[214:217]
	v_mfma_f32_16x16x32_f16 v[94:97], v[206:209], v[160:163], v[30:33]
	v_mfma_f32_16x16x32_f16 v[30:33], v[218:221], v[6:9], v[102:105]
	v_mfma_f32_16x16x32_f16 v[134:137], v[242:245], v[10:13], v[30:33]
	v_mfma_f32_16x16x32_f16 v[30:33], v[218:221], v[14:17], v[98:101]
	v_mfma_f32_16x16x32_f16 v[90:93], v[242:245], v[160:163], v[30:33]
	s_barrier
	ds_read_b128 v[102:105], v150
	ds_read_b128 v[114:117], v151
	ds_read_b128 v[118:121], v152
	ds_read_b128 v[126:129], v153
	s_waitcnt vmcnt(0)
	s_barrier
	s_waitcnt lgkmcnt(0)
	v_mfma_f32_16x16x32_f16 v[30:33], v[18:21], v[102:105], v[222:225]
	v_mfma_f32_16x16x32_f16 v[18:21], v[18:21], v[118:121], v[182:185]
	v_mfma_f32_16x16x32_f16 v[62:65], v[22:25], v[114:117], v[30:33]
	v_mfma_f32_16x16x32_f16 v[30:33], v[22:25], v[126:129], v[18:21]
	v_mfma_f32_16x16x32_f16 v[18:21], v[26:29], v[102:105], v[86:89]
	v_mfma_f32_16x16x32_f16 v[58:61], v[50:53], v[114:117], v[18:21]
	v_mfma_f32_16x16x32_f16 v[18:21], v[26:29], v[118:121], v[82:85]
	v_mfma_f32_16x16x32_f16 v[26:29], v[50:53], v[126:129], v[18:21]
	v_mfma_f32_16x16x32_f16 v[18:21], v[202:205], v[102:105], v[78:81]
	v_mfma_f32_16x16x32_f16 v[54:57], v[206:209], v[114:117], v[18:21]
	v_mfma_f32_16x16x32_f16 v[18:21], v[202:205], v[118:121], v[74:77]
	v_mfma_f32_16x16x32_f16 v[22:25], v[206:209], v[126:129], v[18:21]
	v_mfma_f32_16x16x32_f16 v[18:21], v[218:221], v[102:105], v[70:73]
	v_mfma_f32_16x16x32_f16 v[50:53], v[242:245], v[114:117], v[18:21]
	v_mfma_f32_16x16x32_f16 v[18:21], v[218:221], v[118:121], v[66:69]
	v_mfma_f32_16x16x32_f16 v[18:21], v[242:245], v[126:129], v[18:21]
	s_barrier
	ds_read_b128 v[86:89], v176 offset:49152
	ds_read_b128 v[150:153], v176 offset:50176
	ds_read_b128 v[182:185], v176 offset:51200
	ds_read_b128 v[202:205], v176 offset:52224
	ds_read_b128 v[206:209], v176 offset:53248
	ds_read_b128 v[214:217], v176 offset:54272
	ds_read_b128 v[218:221], v176 offset:55296
	ds_read_b128 v[174:177], v176 offset:56320
	s_barrier
	s_waitcnt lgkmcnt(0)
	v_mfma_f32_16x16x32_f16 v[66:69], v[86:89], v[6:9], v[210:213]
	v_mfma_f32_16x16x32_f16 v[130:133], v[150:153], v[10:13], v[66:69]
	v_mfma_f32_16x16x32_f16 v[66:69], v[86:89], v[14:17], v[226:229]
	v_mfma_f32_16x16x32_f16 v[78:81], v[150:153], v[160:163], v[66:69]
	v_mfma_f32_16x16x32_f16 v[66:69], v[182:185], v[6:9], v[230:233]
	v_mfma_f32_16x16x32_f16 v[46:49], v[206:209], v[6:9], v[46:49]
	v_mfma_f32_16x16x32_f16 v[6:9], v[218:221], v[6:9], v[38:41]
	v_mfma_f32_16x16x32_f16 v[122:125], v[202:205], v[10:13], v[66:69]
	v_mfma_f32_16x16x32_f16 v[66:69], v[182:185], v[14:17], v[234:237]
	v_mfma_f32_16x16x32_f16 v[42:45], v[206:209], v[14:17], v[42:45]
	v_mfma_f32_16x16x32_f16 v[82:85], v[174:177], v[10:13], v[6:9]
	v_mfma_f32_16x16x32_f16 v[6:9], v[218:221], v[14:17], v[34:37]
	v_mfma_f32_16x16x32_f16 v[74:77], v[202:205], v[160:163], v[66:69]
	v_mfma_f32_16x16x32_f16 v[98:101], v[214:217], v[10:13], v[46:49]
	v_mfma_f32_16x16x32_f16 v[70:73], v[214:217], v[160:163], v[42:45]
	v_mfma_f32_16x16x32_f16 v[66:69], v[174:177], v[160:163], v[6:9]
	v_mfma_f32_16x16x32_f16 v[6:9], v[86:89], v[102:105], v[138:141]
	v_mfma_f32_16x16x32_f16 v[46:49], v[150:153], v[114:117], v[6:9]
	v_mfma_f32_16x16x32_f16 v[6:9], v[86:89], v[118:121], v[168:171]
	v_mfma_f32_16x16x32_f16 v[14:17], v[150:153], v[126:129], v[6:9]
	v_mfma_f32_16x16x32_f16 v[6:9], v[182:185], v[102:105], v[238:241]
	v_mfma_f32_16x16x32_f16 v[42:45], v[202:205], v[114:117], v[6:9]
	v_mfma_f32_16x16x32_f16 v[6:9], v[182:185], v[118:121], v[186:189]
	v_mfma_f32_16x16x32_f16 v[10:13], v[202:205], v[126:129], v[6:9]
	v_mfma_f32_16x16x32_f16 v[6:9], v[206:209], v[102:105], v[190:193]
	v_mfma_f32_16x16x32_f16 v[38:41], v[214:217], v[114:117], v[6:9]
	v_mfma_f32_16x16x32_f16 v[6:9], v[206:209], v[118:121], v[194:197]
	v_mfma_f32_16x16x32_f16 v[34:37], v[218:221], v[102:105], v[198:201]
	v_mfma_f32_16x16x32_f16 v[2:5], v[218:221], v[118:121], v[2:5]
	v_mfma_f32_16x16x32_f16 v[6:9], v[214:217], v[126:129], v[6:9]
	v_mfma_f32_16x16x32_f16 v[34:37], v[174:177], v[114:117], v[34:37]
	v_mfma_f32_16x16x32_f16 v[2:5], v[174:177], v[126:129], v[2:5]
	s_cmpk_gt_u32 s62, 0xff
	s_barrier
	s_cbranch_scc1 .LBB8_44
	s_barrier

.LBB9_38:
	ds_read_b128 v[176:179], v169
	ds_read_b128 v[184:187], v171
	ds_read_b128 v[180:183], v170
	ds_read_b128 v[188:191], v172
	v_add_u32_e32 v174, 0xc000, v152
	v_lshl_add_u64 v[192:193], v[136:137], 0, s[42:43]
	v_add_u32_e32 v175, 0xe000, v152
	v_add_u32_e32 v173, s39, v168
	v_lshl_add_u64 v[230:231], v[192:193], 0, s[10:11]
	s_mov_b32 m0, s65
	v_lshl_add_u64 v[246:247], v[134:135], 0, s[42:43]
	ds_read_b128 v[198:201], v173
	ds_read_b128 v[206:209], v173 offset:2048
	ds_read_b128 v[214:217], v173 offset:4096
	ds_read_b128 v[222:225], v173 offset:6144
	ds_read_b128 v[202:205], v173 offset:1024
	ds_read_b128 v[210:213], v173 offset:3072
	ds_read_b128 v[218:221], v173 offset:5120
	ds_read_b128 v[226:229], v173 offset:7168
	global_load_lds_dwordx4 v[230:231], off
	s_mov_b32 m0, s66
	v_lshl_add_u64 v[230:231], v[246:247], 0, s[10:11]
	global_load_lds_dwordx4 v[230:231], off
	s_waitcnt lgkmcnt(8)
	s_barrier
	s_waitcnt lgkmcnt(4)
	v_mfma_f32_16x16x32_f16 v[2:5], v[198:201], v[176:179], v[2:5]
	v_mfma_f32_16x16x32_f16 v[6:9], v[198:201], v[184:187], v[6:9]
	v_mfma_f32_16x16x32_f16 v[10:13], v[206:209], v[176:179], v[10:13]
	v_mfma_f32_16x16x32_f16 v[18:21], v[206:209], v[184:187], v[18:21]
	v_mfma_f32_16x16x32_f16 v[30:33], v[214:217], v[176:179], v[30:33]
	v_mfma_f32_16x16x32_f16 v[42:45], v[214:217], v[184:187], v[42:45]
	v_mfma_f32_16x16x32_f16 v[54:57], v[222:225], v[176:179], v[54:57]
	v_mfma_f32_16x16x32_f16 v[66:69], v[222:225], v[184:187], v[66:69]
	s_waitcnt lgkmcnt(0)
	v_mfma_f32_16x16x32_f16 v[2:5], v[202:205], v[180:183], v[2:5]
	v_mfma_f32_16x16x32_f16 v[6:9], v[202:205], v[188:191], v[6:9]
	v_mfma_f32_16x16x32_f16 v[10:13], v[210:213], v[180:183], v[10:13]
	v_mfma_f32_16x16x32_f16 v[18:21], v[210:213], v[188:191], v[18:21]
	v_mfma_f32_16x16x32_f16 v[30:33], v[218:221], v[180:183], v[30:33]
	v_mfma_f32_16x16x32_f16 v[42:45], v[218:221], v[188:191], v[42:45]
	v_mfma_f32_16x16x32_f16 v[54:57], v[226:229], v[180:183], v[54:57]
	v_mfma_f32_16x16x32_f16 v[66:69], v[226:229], v[188:191], v[66:69]
	s_barrier
	v_lshl_add_u64 v[248:249], v[140:141], 0, s[42:43]
	v_lshl_add_u64 v[250:251], v[248:249], 0, s[26:27]
	s_mov_b32 m0, s67
	ds_read_b128 v[230:233], v161
	ds_read_b128 v[238:241], v163
	ds_read_b128 v[234:237], v162
	ds_read_b128 v[242:245], v164
	global_load_lds_dwordx4 v[250:251], off
	v_lshl_add_u64 v[250:251], v[138:139], 0, s[42:43]
	s_mov_b32 m0, s68
	v_lshl_add_u64 v[252:253], v[250:251], 0, s[26:27]
	global_load_lds_dwordx4 v[252:253], off
	s_barrier
	s_waitcnt lgkmcnt(2)
	v_mfma_f32_16x16x32_f16 v[14:17], v[198:201], v[230:233], v[14:17]
	v_mfma_f32_16x16x32_f16 v[22:25], v[198:201], v[238:241], v[22:25]
	v_mfma_f32_16x16x32_f16 v[34:37], v[206:209], v[230:233], v[34:37]
	v_mfma_f32_16x16x32_f16 v[46:49], v[206:209], v[238:241], v[46:49]
	v_mfma_f32_16x16x32_f16 v[58:61], v[214:217], v[230:233], v[58:61]
	v_mfma_f32_16x16x32_f16 v[70:73], v[214:217], v[238:241], v[70:73]
	v_mfma_f32_16x16x32_f16 v[78:81], v[222:225], v[230:233], v[78:81]
	v_mfma_f32_16x16x32_f16 v[86:89], v[222:225], v[238:241], v[86:89]
	s_waitcnt lgkmcnt(0)
	v_mfma_f32_16x16x32_f16 v[14:17], v[202:205], v[234:237], v[14:17]
	v_mfma_f32_16x16x32_f16 v[22:25], v[202:205], v[242:245], v[22:25]
	v_mfma_f32_16x16x32_f16 v[34:37], v[210:213], v[234:237], v[34:37]
	v_mfma_f32_16x16x32_f16 v[46:49], v[210:213], v[242:245], v[46:49]
	v_mfma_f32_16x16x32_f16 v[58:61], v[218:221], v[234:237], v[58:61]
	v_mfma_f32_16x16x32_f16 v[70:73], v[218:221], v[242:245], v[70:73]
	v_mfma_f32_16x16x32_f16 v[78:81], v[226:229], v[234:237], v[78:81]
	v_mfma_f32_16x16x32_f16 v[86:89], v[226:229], v[242:245], v[86:89]
	v_lshl_add_u64 v[252:253], v[192:193], 0, s[26:27]
	s_mov_b32 m0, s69
	s_barrier
	ds_read_b128 v[198:201], v173 offset:16384
	ds_read_b128 v[206:209], v173 offset:18432
	ds_read_b128 v[214:217], v173 offset:20480
	ds_read_b128 v[222:225], v173 offset:22528
	ds_read_b128 v[202:205], v173 offset:17408
	ds_read_b128 v[210:213], v173 offset:19456
	ds_read_b128 v[218:221], v173 offset:21504
	ds_read_b128 v[226:229], v173 offset:23552
	global_load_lds_dwordx4 v[252:253], off
	s_mov_b32 m0, s70
	v_lshl_add_u64 v[252:253], v[246:247], 0, s[26:27]
	global_load_lds_dwordx4 v[252:253], off
	s_barrier
	s_waitcnt lgkmcnt(4)
	v_mfma_f32_16x16x32_f16 v[26:29], v[198:201], v[176:179], v[26:29]
	v_mfma_f32_16x16x32_f16 v[38:41], v[198:201], v[184:187], v[38:41]
	v_mfma_f32_16x16x32_f16 v[50:53], v[206:209], v[176:179], v[50:53]
	v_mfma_f32_16x16x32_f16 v[62:65], v[206:209], v[184:187], v[62:65]
	v_mfma_f32_16x16x32_f16 v[74:77], v[214:217], v[176:179], v[74:77]
	v_mfma_f32_16x16x32_f16 v[82:85], v[214:217], v[184:187], v[82:85]
	v_mfma_f32_16x16x32_f16 v[90:93], v[222:225], v[176:179], v[90:93]
	v_mfma_f32_16x16x32_f16 v[94:97], v[222:225], v[184:187], v[94:97]
	s_waitcnt lgkmcnt(0)
	v_mfma_f32_16x16x32_f16 v[26:29], v[202:205], v[180:183], v[26:29]
	v_mfma_f32_16x16x32_f16 v[38:41], v[202:205], v[188:191], v[38:41]
	v_mfma_f32_16x16x32_f16 v[50:53], v[210:213], v[180:183], v[50:53]
	v_mfma_f32_16x16x32_f16 v[62:65], v[210:213], v[188:191], v[62:65]
	v_mfma_f32_16x16x32_f16 v[74:77], v[218:221], v[180:183], v[74:77]
	v_mfma_f32_16x16x32_f16 v[82:85], v[218:221], v[188:191], v[82:85]
	v_mfma_f32_16x16x32_f16 v[90:93], v[226:229], v[180:183], v[90:93]
	v_mfma_f32_16x16x32_f16 v[94:97], v[226:229], v[188:191], v[94:97]
	s_barrier
	s_mov_b32 m0, s71
	v_lshl_add_u64 v[176:177], v[248:249], 0, s[28:29]
	global_load_lds_dwordx4 v[176:177], off
	s_mov_b32 m0, s72
	v_lshl_add_u64 v[176:177], v[250:251], 0, s[28:29]
	global_load_lds_dwordx4 v[176:177], off
	s_waitcnt vmcnt(6)
	s_barrier
	v_mfma_f32_16x16x32_f16 v[98:101], v[198:201], v[230:233], v[98:101]
	v_mfma_f32_16x16x32_f16 v[102:105], v[198:201], v[238:241], v[102:105]
	v_mfma_f32_16x16x32_f16 v[106:109], v[206:209], v[230:233], v[106:109]
	v_mfma_f32_16x16x32_f16 v[110:113], v[206:209], v[238:241], v[110:113]
	v_mfma_f32_16x16x32_f16 v[114:117], v[214:217], v[230:233], v[114:117]
	v_mfma_f32_16x16x32_f16 v[118:121], v[214:217], v[238:241], v[118:121]
	v_mfma_f32_16x16x32_f16 v[122:125], v[222:225], v[230:233], v[122:125]
	v_mfma_f32_16x16x32_f16 v[126:129], v[222:225], v[238:241], v[126:129]
	v_mfma_f32_16x16x32_f16 v[98:101], v[202:205], v[234:237], v[98:101]
	v_mfma_f32_16x16x32_f16 v[102:105], v[202:205], v[242:245], v[102:105]
	v_mfma_f32_16x16x32_f16 v[106:109], v[210:213], v[234:237], v[106:109]
	v_mfma_f32_16x16x32_f16 v[110:113], v[210:213], v[242:245], v[110:113]
	v_mfma_f32_16x16x32_f16 v[114:117], v[218:221], v[234:237], v[114:117]
	v_mfma_f32_16x16x32_f16 v[118:121], v[218:221], v[242:245], v[118:121]
	v_mfma_f32_16x16x32_f16 v[122:125], v[226:229], v[234:237], v[122:125]
	v_mfma_f32_16x16x32_f16 v[126:129], v[226:229], v[242:245], v[126:129]
	s_barrier
	ds_read_b128 v[176:179], v144
	ds_read_b128 v[184:187], v150
	ds_read_b128 v[180:183], v145
	ds_read_b128 v[188:191], v151
	v_lshl_add_u64 v[230:231], v[192:193], 0, s[28:29]
	s_mov_b32 m0, s73
	ds_read_b128 v[198:201], v173 offset:32768
	ds_read_b128 v[206:209], v173 offset:34816
	ds_read_b128 v[214:217], v173 offset:36864
	ds_read_b128 v[222:225], v173 offset:38912
	ds_read_b128 v[202:205], v173 offset:33792
	ds_read_b128 v[210:213], v173 offset:35840
	ds_read_b128 v[218:221], v173 offset:37888
	ds_read_b128 v[226:229], v173 offset:39936
	global_load_lds_dwordx4 v[230:231], off
	s_mov_b32 m0, s74
	v_lshl_add_u64 v[230:231], v[246:247], 0, s[28:29]
	global_load_lds_dwordx4 v[230:231], off
	s_waitcnt lgkmcnt(8)
	s_barrier
	s_waitcnt lgkmcnt(4)
	v_mfma_f32_16x16x32_f16 v[2:5], v[198:201], v[176:179], v[2:5]
	v_mfma_f32_16x16x32_f16 v[6:9], v[198:201], v[184:187], v[6:9]
	v_mfma_f32_16x16x32_f16 v[10:13], v[206:209], v[176:179], v[10:13]
	v_mfma_f32_16x16x32_f16 v[18:21], v[206:209], v[184:187], v[18:21]
	v_mfma_f32_16x16x32_f16 v[30:33], v[214:217], v[176:179], v[30:33]
	v_mfma_f32_16x16x32_f16 v[42:45], v[214:217], v[184:187], v[42:45]
	v_mfma_f32_16x16x32_f16 v[54:57], v[222:225], v[176:179], v[54:57]
	v_mfma_f32_16x16x32_f16 v[66:69], v[222:225], v[184:187], v[66:69]
	s_waitcnt lgkmcnt(0)
	v_mfma_f32_16x16x32_f16 v[2:5], v[202:205], v[180:183], v[2:5]
	v_mfma_f32_16x16x32_f16 v[6:9], v[202:205], v[188:191], v[6:9]
	v_mfma_f32_16x16x32_f16 v[10:13], v[210:213], v[180:183], v[10:13]
	v_mfma_f32_16x16x32_f16 v[18:21], v[210:213], v[188:191], v[18:21]
	v_mfma_f32_16x16x32_f16 v[30:33], v[218:221], v[180:183], v[30:33]
	v_mfma_f32_16x16x32_f16 v[42:45], v[218:221], v[188:191], v[42:45]
	v_mfma_f32_16x16x32_f16 v[54:57], v[226:229], v[180:183], v[54:57]
	v_mfma_f32_16x16x32_f16 v[66:69], v[226:229], v[188:191], v[66:69]
	s_barrier
	v_lshl_add_u64 v[252:253], v[248:249], 0, s[30:31]
	s_mov_b32 m0, s75
	ds_read_b128 v[230:233], v146
	ds_read_b128 v[238:241], v148
	ds_read_b128 v[234:237], v147
	ds_read_b128 v[242:245], v149
	global_load_lds_dwordx4 v[252:253], off
	s_mov_b32 m0, s76
	v_lshl_add_u64 v[252:253], v[250:251], 0, s[30:31]
	global_load_lds_dwordx4 v[252:253], off
	s_barrier
	s_waitcnt lgkmcnt(2)
	v_mfma_f32_16x16x32_f16 v[14:17], v[198:201], v[230:233], v[14:17]
	v_mfma_f32_16x16x32_f16 v[22:25], v[198:201], v[238:241], v[22:25]
	v_mfma_f32_16x16x32_f16 v[34:37], v[206:209], v[230:233], v[34:37]
	v_mfma_f32_16x16x32_f16 v[46:49], v[206:209], v[238:241], v[46:49]
	v_mfma_f32_16x16x32_f16 v[58:61], v[214:217], v[230:233], v[58:61]
	v_mfma_f32_16x16x32_f16 v[70:73], v[214:217], v[238:241], v[70:73]
	v_mfma_f32_16x16x32_f16 v[78:81], v[222:225], v[230:233], v[78:81]
	v_mfma_f32_16x16x32_f16 v[86:89], v[222:225], v[238:241], v[86:89]
	s_waitcnt lgkmcnt(0)
	v_mfma_f32_16x16x32_f16 v[14:17], v[202:205], v[234:237], v[14:17]
	v_mfma_f32_16x16x32_f16 v[22:25], v[202:205], v[242:245], v[22:25]
	v_mfma_f32_16x16x32_f16 v[34:37], v[210:213], v[234:237], v[34:37]
	v_mfma_f32_16x16x32_f16 v[46:49], v[210:213], v[242:245], v[46:49]
	v_mfma_f32_16x16x32_f16 v[58:61], v[218:221], v[234:237], v[58:61]
	v_mfma_f32_16x16x32_f16 v[70:73], v[218:221], v[242:245], v[70:73]
	v_mfma_f32_16x16x32_f16 v[78:81], v[226:229], v[234:237], v[78:81]
	v_mfma_f32_16x16x32_f16 v[86:89], v[226:229], v[242:245], v[86:89]
	v_lshl_add_u64 v[192:193], v[192:193], 0, s[30:31]
	s_mov_b32 m0, s77
	s_barrier
	ds_read_b128 v[198:201], v173 offset:49152
	ds_read_b128 v[206:209], v173 offset:51200
	ds_read_b128 v[214:217], v173 offset:53248
	ds_read_b128 v[222:225], v173 offset:55296
	ds_read_b128 v[202:205], v173 offset:50176
	ds_read_b128 v[210:213], v173 offset:52224
	ds_read_b128 v[218:221], v173 offset:54272
	ds_read_b128 v[226:229], v173 offset:56320
	global_load_lds_dwordx4 v[192:193], off
	s_mov_b32 m0, s78
	v_lshl_add_u64 v[192:193], v[246:247], 0, s[30:31]
	global_load_lds_dwordx4 v[192:193], off
	s_barrier
	s_waitcnt lgkmcnt(4)
	v_mfma_f32_16x16x32_f16 v[26:29], v[198:201], v[176:179], v[26:29]
	v_mfma_f32_16x16x32_f16 v[38:41], v[198:201], v[184:187], v[38:41]
	v_mfma_f32_16x16x32_f16 v[50:53], v[206:209], v[176:179], v[50:53]
	v_mfma_f32_16x16x32_f16 v[62:65], v[206:209], v[184:187], v[62:65]
	v_mfma_f32_16x16x32_f16 v[74:77], v[214:217], v[176:179], v[74:77]
	v_mfma_f32_16x16x32_f16 v[82:85], v[214:217], v[184:187], v[82:85]
	v_mfma_f32_16x16x32_f16 v[90:93], v[222:225], v[176:179], v[90:93]
	v_mfma_f32_16x16x32_f16 v[94:97], v[222:225], v[184:187], v[94:97]
	s_waitcnt lgkmcnt(0)
	v_mfma_f32_16x16x32_f16 v[26:29], v[202:205], v[180:183], v[26:29]
	v_mfma_f32_16x16x32_f16 v[38:41], v[202:205], v[188:191], v[38:41]
	v_mfma_f32_16x16x32_f16 v[50:53], v[210:213], v[180:183], v[50:53]
	v_mfma_f32_16x16x32_f16 v[62:65], v[210:213], v[188:191], v[62:65]
	v_mfma_f32_16x16x32_f16 v[74:77], v[218:221], v[180:183], v[74:77]
	v_mfma_f32_16x16x32_f16 v[82:85], v[218:221], v[188:191], v[82:85]
	v_mfma_f32_16x16x32_f16 v[90:93], v[226:229], v[180:183], v[90:93]
	v_mfma_f32_16x16x32_f16 v[94:97], v[226:229], v[188:191], v[94:97]
	s_barrier
	s_mov_b32 m0, s79
	v_lshl_add_u64 v[176:177], v[248:249], 0, s[34:35]
	global_load_lds_dwordx4 v[176:177], off
	s_mov_b32 m0, s80
	v_lshl_add_u64 v[176:177], v[250:251], 0, s[34:35]
	global_load_lds_dwordx4 v[176:177], off
	s_waitcnt vmcnt(6)
	s_barrier
	v_mfma_f32_16x16x32_f16 v[98:101], v[198:201], v[230:233], v[98:101]
	v_mfma_f32_16x16x32_f16 v[102:105], v[198:201], v[238:241], v[102:105]
	v_mfma_f32_16x16x32_f16 v[106:109], v[206:209], v[230:233], v[106:109]
	v_mfma_f32_16x16x32_f16 v[110:113], v[206:209], v[238:241], v[110:113]
	v_mfma_f32_16x16x32_f16 v[114:117], v[214:217], v[230:233], v[114:117]
	v_mfma_f32_16x16x32_f16 v[118:121], v[214:217], v[238:241], v[118:121]
	v_mfma_f32_16x16x32_f16 v[122:125], v[222:225], v[230:233], v[122:125]
	v_mfma_f32_16x16x32_f16 v[126:129], v[222:225], v[238:241], v[126:129]
	v_mfma_f32_16x16x32_f16 v[98:101], v[202:205], v[234:237], v[98:101]
	v_mfma_f32_16x16x32_f16 v[102:105], v[202:205], v[242:245], v[102:105]
	v_mfma_f32_16x16x32_f16 v[106:109], v[210:213], v[234:237], v[106:109]
	v_mfma_f32_16x16x32_f16 v[110:113], v[210:213], v[242:245], v[110:113]
	v_mfma_f32_16x16x32_f16 v[114:117], v[218:221], v[234:237], v[114:117]
	v_mfma_f32_16x16x32_f16 v[118:121], v[218:221], v[242:245], v[118:121]
	v_mfma_f32_16x16x32_f16 v[122:125], v[226:229], v[234:237], v[122:125]
	v_mfma_f32_16x16x32_f16 v[126:129], v[226:229], v[242:245], v[126:129]
	s_add_i32 s44, s44, 2
	s_add_u32 s42, s42, 0x100
	s_addc_u32 s43, s43, 0
	s_cmp_lt_u32 s44, 4
	s_barrier
	s_cbranch_scc1 .LBB9_38
	s_add_u32 s40, s40, 0x20380
	s_addc_u32 s41, s41, 0
	v_readfirstlane_b32 s39, v174
	v_lshl_add_u64 v[130:131], v[130:131], 1, s[40:41]
	s_mov_b32 m0, s39
	v_readfirstlane_b32 s39, v175
	ds_read_b128 v[134:137], v169
	ds_read_b128 v[138:141], v170
	ds_read_b128 v[152:155], v171
	ds_read_b128 v[156:159], v172
	ds_read_b128 v[166:169], v173
	ds_read_b128 v[176:179], v173 offset:1024
	ds_read_b128 v[180:183], v173 offset:2048
	ds_read_b128 v[184:187], v173 offset:3072
	ds_read_b128 v[188:191], v173 offset:4096
	ds_read_b128 v[198:201], v173 offset:5120
	ds_read_b128 v[202:205], v173 offset:6144
	ds_read_b128 v[206:209], v173 offset:7168
	global_load_lds_dwordx4 v[130:131], off
	s_mov_b32 m0, s39
	v_lshl_add_u64 v[130:131], v[132:133], 1, s[40:41]
	global_load_lds_dwordx4 v[130:131], off
	s_barrier
	s_waitcnt lgkmcnt(0)
	v_mfma_f32_16x16x32_f16 v[2:5], v[166:169], v[134:137], v[2:5]
	v_mfma_f32_16x16x32_f16 v[6:9], v[166:169], v[152:155], v[6:9]
	v_mfma_f32_16x16x32_f16 v[30:33], v[188:191], v[134:137], v[30:33]
	v_mfma_f32_16x16x32_f16 v[2:5], v[176:179], v[138:141], v[2:5]
	v_mfma_f32_16x16x32_f16 v[6:9], v[176:179], v[156:159], v[6:9]
	v_mfma_f32_16x16x32_f16 v[10:13], v[180:183], v[134:137], v[10:13]
	v_mfma_f32_16x16x32_f16 v[18:21], v[180:183], v[152:155], v[18:21]
	v_mfma_f32_16x16x32_f16 v[30:33], v[198:201], v[138:141], v[30:33]
	v_mfma_f32_16x16x32_f16 v[42:45], v[188:191], v[152:155], v[42:45]
	v_mfma_f32_16x16x32_f16 v[54:57], v[202:205], v[134:137], v[54:57]
	v_mfma_f32_16x16x32_f16 v[66:69], v[202:205], v[152:155], v[66:69]
	v_mfma_f32_16x16x32_f16 v[10:13], v[184:187], v[138:141], v[10:13]
	v_mfma_f32_16x16x32_f16 v[18:21], v[184:187], v[156:159], v[18:21]
	v_mfma_f32_16x16x32_f16 v[42:45], v[198:201], v[156:159], v[42:45]
	v_mfma_f32_16x16x32_f16 v[54:57], v[206:209], v[138:141], v[54:57]
	v_mfma_f32_16x16x32_f16 v[66:69], v[206:209], v[156:159], v[66:69]
	s_barrier
	ds_read_b128 v[130:133], v161
	ds_read_b128 v[210:213], v162
	ds_read_b128 v[160:163], v163
	ds_read_b128 v[214:217], v164
	s_barrier
	s_waitcnt lgkmcnt(0)
	v_mfma_f32_16x16x32_f16 v[58:61], v[188:191], v[130:133], v[58:61]
	v_mfma_f32_16x16x32_f16 v[14:17], v[166:169], v[130:133], v[14:17]
	v_mfma_f32_16x16x32_f16 v[22:25], v[166:169], v[160:163], v[22:25]
	v_mfma_f32_16x16x32_f16 v[164:167], v[198:201], v[210:213], v[58:61]
	v_mfma_f32_16x16x32_f16 v[58:61], v[188:191], v[160:163], v[70:73]
	v_mfma_f32_16x16x32_f16 v[46:49], v[180:183], v[160:163], v[46:49]
	v_mfma_f32_16x16x32_f16 v[168:171], v[198:201], v[214:217], v[58:61]
	v_mfma_f32_16x16x32_f16 v[58:61], v[202:205], v[130:133], v[78:81]
	v_mfma_f32_16x16x32_f16 v[14:17], v[176:179], v[210:213], v[14:17]
	v_mfma_f32_16x16x32_f16 v[34:37], v[180:183], v[130:133], v[34:37]
	v_mfma_f32_16x16x32_f16 v[46:49], v[184:187], v[214:217], v[46:49]
	v_mfma_f32_16x16x32_f16 v[78:81], v[206:209], v[210:213], v[58:61]
	v_mfma_f32_16x16x32_f16 v[58:61], v[202:205], v[160:163], v[86:89]
	v_mfma_f32_16x16x32_f16 v[22:25], v[176:179], v[214:217], v[22:25]
	v_mfma_f32_16x16x32_f16 v[34:37], v[184:187], v[210:213], v[34:37]
	v_mfma_f32_16x16x32_f16 v[86:89], v[206:209], v[214:217], v[58:61]
	s_barrier
	s_nop 2
	ds_read_b128 v[58:61], v173 offset:16384
	ds_read_b128 v[70:73], v173 offset:17408
	ds_read_b128 v[174:177], v173 offset:18432
	ds_read_b128 v[178:181], v173 offset:19456
	ds_read_b128 v[182:185], v173 offset:20480
	ds_read_b128 v[186:189], v173 offset:21504
	ds_read_b128 v[190:193], v173 offset:22528
	ds_read_b128 v[198:201], v173 offset:23552
	s_waitcnt vmcnt(4)
	s_barrier
	s_waitcnt lgkmcnt(0)
	v_mfma_f32_16x16x32_f16 v[26:29], v[58:61], v[134:137], v[26:29]
	v_mfma_f32_16x16x32_f16 v[26:29], v[70:73], v[138:141], v[26:29]
	v_mfma_f32_16x16x32_f16 v[38:41], v[58:61], v[152:155], v[38:41]
	v_mfma_f32_16x16x32_f16 v[50:53], v[174:177], v[134:137], v[50:53]
	v_mfma_f32_16x16x32_f16 v[62:65], v[174:177], v[152:155], v[62:65]
	v_mfma_f32_16x16x32_f16 v[74:77], v[182:185], v[134:137], v[74:77]
	v_mfma_f32_16x16x32_f16 v[82:85], v[182:185], v[152:155], v[82:85]
	v_mfma_f32_16x16x32_f16 v[90:93], v[190:193], v[134:137], v[90:93]
	v_mfma_f32_16x16x32_f16 v[94:97], v[190:193], v[152:155], v[94:97]
	v_mfma_f32_16x16x32_f16 v[38:41], v[70:73], v[156:159], v[38:41]
	v_mfma_f32_16x16x32_f16 v[50:53], v[178:181], v[138:141], v[50:53]
	v_mfma_f32_16x16x32_f16 v[62:65], v[178:181], v[156:159], v[62:65]
	v_mfma_f32_16x16x32_f16 v[74:77], v[186:189], v[138:141], v[74:77]
	v_mfma_f32_16x16x32_f16 v[82:85], v[186:189], v[156:159], v[82:85]
	v_mfma_f32_16x16x32_f16 v[90:93], v[198:201], v[138:141], v[90:93]
	v_mfma_f32_16x16x32_f16 v[94:97], v[198:201], v[156:159], v[94:97]
	v_mfma_f32_16x16x32_f16 v[98:101], v[58:61], v[130:133], v[98:101]
	v_mfma_f32_16x16x32_f16 v[58:61], v[58:61], v[160:163], v[102:105]
	v_mfma_f32_16x16x32_f16 v[102:105], v[70:73], v[214:217], v[58:61]
	v_mfma_f32_16x16x32_f16 v[58:61], v[174:177], v[130:133], v[106:109]
	v_mfma_f32_16x16x32_f16 v[106:109], v[178:181], v[210:213], v[58:61]
	v_mfma_f32_16x16x32_f16 v[58:61], v[174:177], v[160:163], v[110:113]
	v_mfma_f32_16x16x32_f16 v[202:205], v[178:181], v[214:217], v[58:61]
	v_mfma_f32_16x16x32_f16 v[58:61], v[182:185], v[130:133], v[114:117]
	v_mfma_f32_16x16x32_f16 v[206:209], v[186:189], v[210:213], v[58:61]
	v_mfma_f32_16x16x32_f16 v[58:61], v[182:185], v[160:163], v[118:121]
	v_mfma_f32_16x16x32_f16 v[218:221], v[186:189], v[214:217], v[58:61]
	v_mfma_f32_16x16x32_f16 v[58:61], v[190:193], v[130:133], v[122:125]
	v_mfma_f32_16x16x32_f16 v[98:101], v[70:73], v[210:213], v[98:101]
	v_mfma_f32_16x16x32_f16 v[210:213], v[198:201], v[210:213], v[58:61]
	v_mfma_f32_16x16x32_f16 v[58:61], v[190:193], v[160:163], v[126:129]
	v_mfma_f32_16x16x32_f16 v[198:201], v[198:201], v[214:217], v[58:61]
	s_barrier
	ds_read_b128 v[110:113], v144
	ds_read_b128 v[130:133], v145
	ds_read_b128 v[214:217], v150
	ds_read_b128 v[222:225], v151
	s_nop 0
	ds_read_b128 v[58:61], v173 offset:32768
	ds_read_b128 v[70:73], v173 offset:33792
	ds_read_b128 v[114:117], v173 offset:34816
	ds_read_b128 v[118:121], v173 offset:35840
	ds_read_b128 v[134:137], v173 offset:36864
	ds_read_b128 v[138:141], v173 offset:37888
	ds_read_b128 v[178:181], v173 offset:38912
	ds_read_b128 v[226:229], v173 offset:39936
	s_waitcnt vmcnt(2)
	s_barrier
	s_waitcnt lgkmcnt(0)
	v_mfma_f32_16x16x32_f16 v[2:5], v[58:61], v[110:113], v[2:5]
	v_mfma_f32_16x16x32_f16 v[190:193], v[70:73], v[130:133], v[2:5]
	v_mfma_f32_16x16x32_f16 v[2:5], v[58:61], v[214:217], v[6:9]
	v_mfma_f32_16x16x32_f16 v[158:161], v[70:73], v[222:225], v[2:5]
	v_mfma_f32_16x16x32_f16 v[2:5], v[114:117], v[110:113], v[10:13]
	v_mfma_f32_16x16x32_f16 v[186:189], v[118:121], v[130:133], v[2:5]
	v_mfma_f32_16x16x32_f16 v[2:5], v[114:117], v[214:217], v[18:21]
	v_mfma_f32_16x16x32_f16 v[154:157], v[118:121], v[222:225], v[2:5]
	v_mfma_f32_16x16x32_f16 v[2:5], v[134:137], v[110:113], v[30:33]
	v_mfma_f32_16x16x32_f16 v[182:185], v[138:141], v[130:133], v[2:5]
	v_mfma_f32_16x16x32_f16 v[2:5], v[134:137], v[214:217], v[42:45]
	v_mfma_f32_16x16x32_f16 v[150:153], v[138:141], v[222:225], v[2:5]
	v_mfma_f32_16x16x32_f16 v[2:5], v[178:181], v[110:113], v[54:57]
	v_mfma_f32_16x16x32_f16 v[174:177], v[226:229], v[130:133], v[2:5]
	v_mfma_f32_16x16x32_f16 v[2:5], v[178:181], v[214:217], v[66:69]
	v_mfma_f32_16x16x32_f16 v[142:145], v[226:229], v[222:225], v[2:5]
	s_barrier
	s_nop 4
	ds_read_b128 v[2:5], v146
	ds_read_b128 v[10:13], v147
	ds_read_b128 v[18:21], v148
	ds_read_b128 v[42:45], v149
	s_waitcnt vmcnt(0)
	s_barrier
	s_waitcnt lgkmcnt(0)
	v_mfma_f32_16x16x32_f16 v[6:9], v[58:61], v[2:5], v[14:17]
	v_mfma_f32_16x16x32_f16 v[126:129], v[70:73], v[10:13], v[6:9]
	v_mfma_f32_16x16x32_f16 v[6:9], v[58:61], v[18:21], v[22:25]
	v_mfma_f32_16x16x32_f16 v[70:73], v[70:73], v[42:45], v[6:9]
	v_mfma_f32_16x16x32_f16 v[6:9], v[114:117], v[2:5], v[34:37]
	v_mfma_f32_16x16x32_f16 v[122:125], v[118:121], v[10:13], v[6:9]
	v_mfma_f32_16x16x32_f16 v[6:9], v[114:117], v[18:21], v[46:49]
	v_mfma_f32_16x16x32_f16 v[58:61], v[118:121], v[42:45], v[6:9]
	v_mfma_f32_16x16x32_f16 v[6:9], v[134:137], v[2:5], v[164:167]
	v_mfma_f32_16x16x32_f16 v[118:121], v[138:141], v[10:13], v[6:9]
	v_mfma_f32_16x16x32_f16 v[6:9], v[134:137], v[18:21], v[168:171]
	v_mfma_f32_16x16x32_f16 v[46:49], v[138:141], v[42:45], v[6:9]
	v_mfma_f32_16x16x32_f16 v[6:9], v[178:181], v[2:5], v[78:81]
	v_mfma_f32_16x16x32_f16 v[114:117], v[226:229], v[10:13], v[6:9]
	v_mfma_f32_16x16x32_f16 v[6:9], v[178:181], v[18:21], v[86:89]
	v_mfma_f32_16x16x32_f16 v[30:33], v[226:229], v[42:45], v[6:9]
	s_barrier
	s_nop 4
	ds_read_b128 v[6:9], v173 offset:49152
	ds_read_b128 v[14:17], v173 offset:50176
	ds_read_b128 v[22:25], v173 offset:51200
	ds_read_b128 v[34:37], v173 offset:52224
	ds_read_b128 v[54:57], v173 offset:53248
	ds_read_b128 v[66:69], v173 offset:54272
	ds_read_b128 v[78:81], v173 offset:55296
	ds_read_b128 v[86:89], v173 offset:56320
	s_barrier
	s_waitcnt lgkmcnt(0)
	v_mfma_f32_16x16x32_f16 v[26:29], v[6:9], v[110:113], v[26:29]
	v_mfma_f32_16x16x32_f16 v[178:181], v[14:17], v[130:133], v[26:29]
	v_mfma_f32_16x16x32_f16 v[26:29], v[6:9], v[214:217], v[38:41]
	v_mfma_f32_16x16x32_f16 v[146:149], v[14:17], v[222:225], v[26:29]
	v_mfma_f32_16x16x32_f16 v[26:29], v[22:25], v[110:113], v[50:53]
	v_mfma_f32_16x16x32_f16 v[170:173], v[34:37], v[130:133], v[26:29]
	v_mfma_f32_16x16x32_f16 v[26:29], v[22:25], v[214:217], v[62:65]
	v_mfma_f32_16x16x32_f16 v[138:141], v[34:37], v[222:225], v[26:29]
	v_mfma_f32_16x16x32_f16 v[26:29], v[54:57], v[110:113], v[74:77]
	v_mfma_f32_16x16x32_f16 v[166:169], v[66:69], v[130:133], v[26:29]
	v_mfma_f32_16x16x32_f16 v[26:29], v[54:57], v[214:217], v[82:85]
	v_mfma_f32_16x16x32_f16 v[134:137], v[66:69], v[222:225], v[26:29]
	v_mfma_f32_16x16x32_f16 v[26:29], v[78:81], v[110:113], v[90:93]
	v_mfma_f32_16x16x32_f16 v[162:165], v[86:89], v[130:133], v[26:29]
	v_mfma_f32_16x16x32_f16 v[26:29], v[78:81], v[214:217], v[94:97]
	v_mfma_f32_16x16x32_f16 v[130:133], v[86:89], v[222:225], v[26:29]
	v_mfma_f32_16x16x32_f16 v[26:29], v[6:9], v[2:5], v[98:101]
	v_mfma_f32_16x16x32_f16 v[6:9], v[6:9], v[18:21], v[102:105]
	v_mfma_f32_16x16x32_f16 v[110:113], v[14:17], v[10:13], v[26:29]
	v_mfma_f32_16x16x32_f16 v[26:29], v[14:17], v[42:45], v[6:9]
	v_mfma_f32_16x16x32_f16 v[6:9], v[22:25], v[2:5], v[106:109]
	v_mfma_f32_16x16x32_f16 v[106:109], v[34:37], v[10:13], v[6:9]
	v_mfma_f32_16x16x32_f16 v[6:9], v[22:25], v[18:21], v[202:205]
	v_mfma_f32_16x16x32_f16 v[14:17], v[34:37], v[42:45], v[6:9]
	v_mfma_f32_16x16x32_f16 v[6:9], v[54:57], v[2:5], v[206:209]
	v_mfma_f32_16x16x32_f16 v[2:5], v[78:81], v[2:5], v[210:213]
	v_mfma_f32_16x16x32_f16 v[102:105], v[66:69], v[10:13], v[6:9]
	v_mfma_f32_16x16x32_f16 v[6:9], v[54:57], v[18:21], v[218:221]
	v_mfma_f32_16x16x32_f16 v[98:101], v[86:89], v[10:13], v[2:5]
	v_mfma_f32_16x16x32_f16 v[2:5], v[78:81], v[18:21], v[198:201]
	v_mfma_f32_16x16x32_f16 v[6:9], v[66:69], v[42:45], v[6:9]
	v_mfma_f32_16x16x32_f16 v[2:5], v[86:89], v[42:45], v[2:5]
	s_cmpk_gt_u32 s54, 0xff
	s_barrier
	s_cbranch_scc1 .LBB9_34
	s_barrier
	s_branch .LBB9_34

.LBB10_12:
	ds_read_b128 v[182:185], v171
	ds_read_b128 v[190:193], v174
	ds_read_b128 v[186:189], v173
	ds_read_b128 v[194:197], v175
	v_add_u32_e32 v177, 0xc000, v148
	v_lshl_add_u64 v[246:247], v[136:137], 0, s[44:45]
	v_add_u32_e32 v176, s63, v170
	v_lshl_add_u64 v[178:179], v[246:247], 0, s[28:29]
	s_mov_b32 m0, s70
	ds_read_b128 v[198:201], v176
	ds_read_b128 v[206:209], v176 offset:2048
	ds_read_b128 v[214:217], v176 offset:4096
	ds_read_b128 v[222:225], v176 offset:6144
	ds_read_b128 v[202:205], v176 offset:1024
	ds_read_b128 v[210:213], v176 offset:3072
	ds_read_b128 v[218:221], v176 offset:5120
	ds_read_b128 v[226:229], v176 offset:7168
	global_load_lds_dwordx4 v[178:179], off
	v_add_u32_e32 v178, 0xe000, v148
	v_lshl_add_u64 v[248:249], v[134:135], 0, s[44:45]
	s_mov_b32 m0, s71
	v_lshl_add_u64 v[230:231], v[248:249], 0, s[28:29]
	global_load_lds_dwordx4 v[230:231], off
	s_waitcnt lgkmcnt(8)
	s_barrier
	s_waitcnt lgkmcnt(4)
	v_mfma_f32_16x16x32_f16 v[126:129], v[198:201], v[182:185], v[126:129]
	v_mfma_f32_16x16x32_f16 v[122:125], v[198:201], v[190:193], v[122:125]
	v_mfma_f32_16x16x32_f16 v[118:121], v[206:209], v[182:185], v[118:121]
	v_mfma_f32_16x16x32_f16 v[114:117], v[206:209], v[190:193], v[114:117]
	v_mfma_f32_16x16x32_f16 v[110:113], v[214:217], v[182:185], v[110:113]
	v_mfma_f32_16x16x32_f16 v[106:109], v[214:217], v[190:193], v[106:109]
	v_mfma_f32_16x16x32_f16 v[102:105], v[222:225], v[182:185], v[102:105]
	v_mfma_f32_16x16x32_f16 v[98:101], v[222:225], v[190:193], v[98:101]
	s_waitcnt lgkmcnt(0)
	v_mfma_f32_16x16x32_f16 v[126:129], v[202:205], v[186:189], v[126:129]
	v_mfma_f32_16x16x32_f16 v[122:125], v[202:205], v[194:197], v[122:125]
	v_mfma_f32_16x16x32_f16 v[118:121], v[210:213], v[186:189], v[118:121]
	v_mfma_f32_16x16x32_f16 v[114:117], v[210:213], v[194:197], v[114:117]
	v_mfma_f32_16x16x32_f16 v[110:113], v[218:221], v[186:189], v[110:113]
	v_mfma_f32_16x16x32_f16 v[106:109], v[218:221], v[194:197], v[106:109]
	v_mfma_f32_16x16x32_f16 v[102:105], v[226:229], v[186:189], v[102:105]
	v_mfma_f32_16x16x32_f16 v[98:101], v[226:229], v[194:197], v[98:101]
	s_barrier
	v_lshl_add_u64 v[250:251], v[140:141], 0, s[44:45]
	v_lshl_add_u64 v[252:253], v[250:251], 0, s[30:31]
	s_mov_b32 m0, s72
	ds_read_b128 v[230:233], v162
	ds_read_b128 v[238:241], v164
	ds_read_b128 v[234:237], v163
	ds_read_b128 v[242:245], v165
	global_load_lds_dwordx4 v[252:253], off
	v_lshl_add_u64 v[252:253], v[138:139], 0, s[44:45]
	s_mov_b32 m0, s73
	v_lshl_add_u64 v[254:255], v[252:253], 0, s[30:31]
	global_load_lds_dwordx4 v[254:255], off
	s_barrier
	s_waitcnt lgkmcnt(2)
	v_mfma_f32_16x16x32_f16 v[94:97], v[198:201], v[230:233], v[94:97]
	v_mfma_f32_16x16x32_f16 v[90:93], v[198:201], v[238:241], v[90:93]
	v_mfma_f32_16x16x32_f16 v[86:89], v[206:209], v[230:233], v[86:89]
	v_mfma_f32_16x16x32_f16 v[82:85], v[206:209], v[238:241], v[82:85]
	v_mfma_f32_16x16x32_f16 v[78:81], v[214:217], v[230:233], v[78:81]
	v_mfma_f32_16x16x32_f16 v[74:77], v[214:217], v[238:241], v[74:77]
	v_mfma_f32_16x16x32_f16 v[70:73], v[222:225], v[230:233], v[70:73]
	v_mfma_f32_16x16x32_f16 v[66:69], v[222:225], v[238:241], v[66:69]
	s_waitcnt lgkmcnt(0)
	v_mfma_f32_16x16x32_f16 v[94:97], v[202:205], v[234:237], v[94:97]
	v_mfma_f32_16x16x32_f16 v[90:93], v[202:205], v[242:245], v[90:93]
	v_mfma_f32_16x16x32_f16 v[86:89], v[210:213], v[234:237], v[86:89]
	v_mfma_f32_16x16x32_f16 v[82:85], v[210:213], v[242:245], v[82:85]
	v_mfma_f32_16x16x32_f16 v[78:81], v[218:221], v[234:237], v[78:81]
	v_mfma_f32_16x16x32_f16 v[74:77], v[218:221], v[242:245], v[74:77]
	v_mfma_f32_16x16x32_f16 v[70:73], v[226:229], v[234:237], v[70:73]
	v_mfma_f32_16x16x32_f16 v[66:69], v[226:229], v[242:245], v[66:69]
	v_lshl_add_u64 v[254:255], v[246:247], 0, s[30:31]
	s_mov_b32 m0, s74
	s_barrier
	ds_read_b128 v[198:201], v176 offset:16384
	ds_read_b128 v[206:209], v176 offset:18432
	ds_read_b128 v[214:217], v176 offset:20480
	ds_read_b128 v[222:225], v176 offset:22528
	ds_read_b128 v[202:205], v176 offset:17408
	ds_read_b128 v[210:213], v176 offset:19456
	ds_read_b128 v[218:221], v176 offset:21504
	ds_read_b128 v[226:229], v176 offset:23552
	global_load_lds_dwordx4 v[254:255], off
	s_mov_b32 m0, s75
	v_lshl_add_u64 v[254:255], v[248:249], 0, s[30:31]
	global_load_lds_dwordx4 v[254:255], off
	s_barrier
	s_waitcnt lgkmcnt(4)
	v_mfma_f32_16x16x32_f16 v[62:65], v[198:201], v[182:185], v[62:65]
	v_mfma_f32_16x16x32_f16 v[58:61], v[198:201], v[190:193], v[58:61]
	v_mfma_f32_16x16x32_f16 v[54:57], v[206:209], v[182:185], v[54:57]
	v_mfma_f32_16x16x32_f16 v[50:53], v[206:209], v[190:193], v[50:53]
	v_mfma_f32_16x16x32_f16 v[46:49], v[214:217], v[182:185], v[46:49]
	v_mfma_f32_16x16x32_f16 v[42:45], v[214:217], v[190:193], v[42:45]
	v_mfma_f32_16x16x32_f16 v[38:41], v[222:225], v[182:185], v[38:41]
	v_mfma_f32_16x16x32_f16 v[34:37], v[222:225], v[190:193], v[34:37]
	s_waitcnt lgkmcnt(0)
	v_mfma_f32_16x16x32_f16 v[62:65], v[202:205], v[186:189], v[62:65]
	v_mfma_f32_16x16x32_f16 v[58:61], v[202:205], v[194:197], v[58:61]
	v_mfma_f32_16x16x32_f16 v[54:57], v[210:213], v[186:189], v[54:57]
	v_mfma_f32_16x16x32_f16 v[50:53], v[210:213], v[194:197], v[50:53]
	v_mfma_f32_16x16x32_f16 v[46:49], v[218:221], v[186:189], v[46:49]
	v_mfma_f32_16x16x32_f16 v[42:45], v[218:221], v[194:197], v[42:45]
	v_mfma_f32_16x16x32_f16 v[38:41], v[226:229], v[186:189], v[38:41]
	v_mfma_f32_16x16x32_f16 v[34:37], v[226:229], v[194:197], v[34:37]
	s_barrier
	s_mov_b32 m0, s76
	v_lshl_add_u64 v[182:183], v[250:251], 0, s[34:35]
	global_load_lds_dwordx4 v[182:183], off
	s_mov_b32 m0, s77
	v_lshl_add_u64 v[182:183], v[252:253], 0, s[34:35]
	global_load_lds_dwordx4 v[182:183], off
	s_waitcnt vmcnt(6)
	s_barrier
	v_mfma_f32_16x16x32_f16 v[30:33], v[198:201], v[230:233], v[30:33]
	v_mfma_f32_16x16x32_f16 v[26:29], v[198:201], v[238:241], v[26:29]
	v_mfma_f32_16x16x32_f16 v[22:25], v[206:209], v[230:233], v[22:25]
	v_mfma_f32_16x16x32_f16 v[18:21], v[206:209], v[238:241], v[18:21]
	v_mfma_f32_16x16x32_f16 v[14:17], v[214:217], v[230:233], v[14:17]
	v_mfma_f32_16x16x32_f16 v[10:13], v[214:217], v[238:241], v[10:13]
	v_mfma_f32_16x16x32_f16 v[6:9], v[222:225], v[230:233], v[6:9]
	v_mfma_f32_16x16x32_f16 v[2:5], v[222:225], v[238:241], v[2:5]
	v_mfma_f32_16x16x32_f16 v[30:33], v[202:205], v[234:237], v[30:33]
	v_mfma_f32_16x16x32_f16 v[26:29], v[202:205], v[242:245], v[26:29]
	v_mfma_f32_16x16x32_f16 v[22:25], v[210:213], v[234:237], v[22:25]
	v_mfma_f32_16x16x32_f16 v[18:21], v[210:213], v[242:245], v[18:21]
	v_mfma_f32_16x16x32_f16 v[14:17], v[218:221], v[234:237], v[14:17]
	v_mfma_f32_16x16x32_f16 v[10:13], v[218:221], v[242:245], v[10:13]
	v_mfma_f32_16x16x32_f16 v[6:9], v[226:229], v[234:237], v[6:9]
	v_mfma_f32_16x16x32_f16 v[2:5], v[226:229], v[242:245], v[2:5]
	s_barrier
	ds_read_b128 v[182:185], v144
	ds_read_b128 v[190:193], v146
	ds_read_b128 v[186:189], v145
	ds_read_b128 v[194:197], v147
	v_lshl_add_u64 v[230:231], v[246:247], 0, s[34:35]
	s_mov_b32 m0, s78
	ds_read_b128 v[198:201], v176 offset:32768
	ds_read_b128 v[206:209], v176 offset:34816
	ds_read_b128 v[214:217], v176 offset:36864
	ds_read_b128 v[222:225], v176 offset:38912
	ds_read_b128 v[202:205], v176 offset:33792
	ds_read_b128 v[210:213], v176 offset:35840
	ds_read_b128 v[218:221], v176 offset:37888
	ds_read_b128 v[226:229], v176 offset:39936
	global_load_lds_dwordx4 v[230:231], off
	s_mov_b32 m0, s79
	v_lshl_add_u64 v[230:231], v[248:249], 0, s[34:35]
	global_load_lds_dwordx4 v[230:231], off
	s_waitcnt lgkmcnt(8)
	s_barrier
	s_waitcnt lgkmcnt(4)
	v_mfma_f32_16x16x32_f16 v[126:129], v[198:201], v[182:185], v[126:129]
	v_mfma_f32_16x16x32_f16 v[122:125], v[198:201], v[190:193], v[122:125]
	v_mfma_f32_16x16x32_f16 v[118:121], v[206:209], v[182:185], v[118:121]
	v_mfma_f32_16x16x32_f16 v[114:117], v[206:209], v[190:193], v[114:117]
	v_mfma_f32_16x16x32_f16 v[110:113], v[214:217], v[182:185], v[110:113]
	v_mfma_f32_16x16x32_f16 v[106:109], v[214:217], v[190:193], v[106:109]
	v_mfma_f32_16x16x32_f16 v[102:105], v[222:225], v[182:185], v[102:105]
	v_mfma_f32_16x16x32_f16 v[98:101], v[222:225], v[190:193], v[98:101]
	s_waitcnt lgkmcnt(0)
	v_mfma_f32_16x16x32_f16 v[126:129], v[202:205], v[186:189], v[126:129]
	v_mfma_f32_16x16x32_f16 v[122:125], v[202:205], v[194:197], v[122:125]
	v_mfma_f32_16x16x32_f16 v[118:121], v[210:213], v[186:189], v[118:121]
	v_mfma_f32_16x16x32_f16 v[114:117], v[210:213], v[194:197], v[114:117]
	v_mfma_f32_16x16x32_f16 v[110:113], v[218:221], v[186:189], v[110:113]
	v_mfma_f32_16x16x32_f16 v[106:109], v[218:221], v[194:197], v[106:109]
	v_mfma_f32_16x16x32_f16 v[102:105], v[226:229], v[186:189], v[102:105]
	v_mfma_f32_16x16x32_f16 v[98:101], v[226:229], v[194:197], v[98:101]
	s_barrier
	v_lshl_add_u64 v[254:255], v[250:251], 0, s[36:37]
	s_mov_b32 m0, s80
	ds_read_b128 v[230:233], v150
	ds_read_b128 v[238:241], v152
	ds_read_b128 v[234:237], v151
	ds_read_b128 v[242:245], v153
	global_load_lds_dwordx4 v[254:255], off
	s_mov_b32 m0, s81
	v_lshl_add_u64 v[254:255], v[252:253], 0, s[36:37]
	global_load_lds_dwordx4 v[254:255], off
	s_barrier
	s_waitcnt lgkmcnt(2)
	v_mfma_f32_16x16x32_f16 v[94:97], v[198:201], v[230:233], v[94:97]
	v_mfma_f32_16x16x32_f16 v[90:93], v[198:201], v[238:241], v[90:93]
	v_mfma_f32_16x16x32_f16 v[86:89], v[206:209], v[230:233], v[86:89]
	v_mfma_f32_16x16x32_f16 v[82:85], v[206:209], v[238:241], v[82:85]
	v_mfma_f32_16x16x32_f16 v[78:81], v[214:217], v[230:233], v[78:81]
	v_mfma_f32_16x16x32_f16 v[74:77], v[214:217], v[238:241], v[74:77]
	v_mfma_f32_16x16x32_f16 v[70:73], v[222:225], v[230:233], v[70:73]
	v_mfma_f32_16x16x32_f16 v[66:69], v[222:225], v[238:241], v[66:69]
	s_waitcnt lgkmcnt(0)
	v_mfma_f32_16x16x32_f16 v[94:97], v[202:205], v[234:237], v[94:97]
	v_mfma_f32_16x16x32_f16 v[90:93], v[202:205], v[242:245], v[90:93]
	v_mfma_f32_16x16x32_f16 v[86:89], v[210:213], v[234:237], v[86:89]
	v_mfma_f32_16x16x32_f16 v[82:85], v[210:213], v[242:245], v[82:85]
	v_mfma_f32_16x16x32_f16 v[78:81], v[218:221], v[234:237], v[78:81]
	v_mfma_f32_16x16x32_f16 v[74:77], v[218:221], v[242:245], v[74:77]
	v_mfma_f32_16x16x32_f16 v[70:73], v[226:229], v[234:237], v[70:73]
	v_mfma_f32_16x16x32_f16 v[66:69], v[226:229], v[242:245], v[66:69]
	v_lshl_add_u64 v[246:247], v[246:247], 0, s[36:37]
	s_mov_b32 m0, s82
	s_barrier
	ds_read_b128 v[198:201], v176 offset:49152
	ds_read_b128 v[206:209], v176 offset:51200
	ds_read_b128 v[214:217], v176 offset:53248
	ds_read_b128 v[222:225], v176 offset:55296
	ds_read_b128 v[202:205], v176 offset:50176
	ds_read_b128 v[210:213], v176 offset:52224
	ds_read_b128 v[218:221], v176 offset:54272
	ds_read_b128 v[226:229], v176 offset:56320
	global_load_lds_dwordx4 v[246:247], off
	s_mov_b32 m0, s83
	v_lshl_add_u64 v[246:247], v[248:249], 0, s[36:37]
	global_load_lds_dwordx4 v[246:247], off
	s_barrier
	s_waitcnt lgkmcnt(4)
	v_mfma_f32_16x16x32_f16 v[62:65], v[198:201], v[182:185], v[62:65]
	v_mfma_f32_16x16x32_f16 v[58:61], v[198:201], v[190:193], v[58:61]
	v_mfma_f32_16x16x32_f16 v[54:57], v[206:209], v[182:185], v[54:57]
	v_mfma_f32_16x16x32_f16 v[50:53], v[206:209], v[190:193], v[50:53]
	v_mfma_f32_16x16x32_f16 v[46:49], v[214:217], v[182:185], v[46:49]
	v_mfma_f32_16x16x32_f16 v[42:45], v[214:217], v[190:193], v[42:45]
	v_mfma_f32_16x16x32_f16 v[38:41], v[222:225], v[182:185], v[38:41]
	v_mfma_f32_16x16x32_f16 v[34:37], v[222:225], v[190:193], v[34:37]
	s_waitcnt lgkmcnt(0)
	v_mfma_f32_16x16x32_f16 v[62:65], v[202:205], v[186:189], v[62:65]
	v_mfma_f32_16x16x32_f16 v[58:61], v[202:205], v[194:197], v[58:61]
	v_mfma_f32_16x16x32_f16 v[54:57], v[210:213], v[186:189], v[54:57]
	v_mfma_f32_16x16x32_f16 v[50:53], v[210:213], v[194:197], v[50:53]
	v_mfma_f32_16x16x32_f16 v[46:49], v[218:221], v[186:189], v[46:49]
	v_mfma_f32_16x16x32_f16 v[42:45], v[218:221], v[194:197], v[42:45]
	v_mfma_f32_16x16x32_f16 v[38:41], v[226:229], v[186:189], v[38:41]
	v_mfma_f32_16x16x32_f16 v[34:37], v[226:229], v[194:197], v[34:37]
	s_barrier
	s_mov_b32 m0, s84
	v_lshl_add_u64 v[182:183], v[250:251], 0, s[38:39]
	global_load_lds_dwordx4 v[182:183], off
	s_mov_b32 m0, s85
	v_lshl_add_u64 v[182:183], v[252:253], 0, s[38:39]
	global_load_lds_dwordx4 v[182:183], off
	s_waitcnt vmcnt(6)
	s_barrier
	v_mfma_f32_16x16x32_f16 v[30:33], v[198:201], v[230:233], v[30:33]
	v_mfma_f32_16x16x32_f16 v[26:29], v[198:201], v[238:241], v[26:29]
	v_mfma_f32_16x16x32_f16 v[22:25], v[206:209], v[230:233], v[22:25]
	v_mfma_f32_16x16x32_f16 v[18:21], v[206:209], v[238:241], v[18:21]
	v_mfma_f32_16x16x32_f16 v[14:17], v[214:217], v[230:233], v[14:17]
	v_mfma_f32_16x16x32_f16 v[10:13], v[214:217], v[238:241], v[10:13]
	v_mfma_f32_16x16x32_f16 v[6:9], v[222:225], v[230:233], v[6:9]
	v_mfma_f32_16x16x32_f16 v[2:5], v[222:225], v[238:241], v[2:5]
	v_mfma_f32_16x16x32_f16 v[30:33], v[202:205], v[234:237], v[30:33]
	v_mfma_f32_16x16x32_f16 v[26:29], v[202:205], v[242:245], v[26:29]
	v_mfma_f32_16x16x32_f16 v[22:25], v[210:213], v[234:237], v[22:25]
	v_mfma_f32_16x16x32_f16 v[18:21], v[210:213], v[242:245], v[18:21]
	v_mfma_f32_16x16x32_f16 v[14:17], v[218:221], v[234:237], v[14:17]
	v_mfma_f32_16x16x32_f16 v[10:13], v[218:221], v[242:245], v[10:13]
	v_mfma_f32_16x16x32_f16 v[6:9], v[226:229], v[234:237], v[6:9]
	v_mfma_f32_16x16x32_f16 v[2:5], v[226:229], v[242:245], v[2:5]
	s_add_i32 s46, s46, 2
	s_add_u32 s44, s44, 0x100
	s_addc_u32 s45, s45, 0
	s_cmp_lt_u32 s46, 28
	s_barrier
	s_cbranch_scc1 .LBB10_12
	s_add_u32 s42, s42, 0x80f80
	s_addc_u32 s43, s43, 0
	v_readfirstlane_b32 s44, v177
	v_lshl_add_u64 v[130:131], v[130:131], 1, s[42:43]
	s_mov_b32 m0, s44
	ds_read_b128 v[134:137], v171
	ds_read_b128 v[138:141], v173
	ds_read_b128 v[154:157], v174
	ds_read_b128 v[168:171], v175
	ds_read_b128 v[182:185], v176
	ds_read_b128 v[186:189], v176 offset:1024
	ds_read_b128 v[190:193], v176 offset:2048
	ds_read_b128 v[194:197], v176 offset:3072
	ds_read_b128 v[198:201], v176 offset:4096
	ds_read_b128 v[202:205], v176 offset:5120
	ds_read_b128 v[206:209], v176 offset:6144
	ds_read_b128 v[210:213], v176 offset:7168
	global_load_lds_dwordx4 v[130:131], off
	v_lshl_add_u64 v[130:131], v[132:133], 1, s[42:43]
	v_readfirstlane_b32 s42, v178
	s_mov_b32 m0, s42
	s_nop 0
	global_load_lds_dwordx4 v[130:131], off
	s_barrier
	s_waitcnt lgkmcnt(0)
	v_mfma_f32_16x16x32_f16 v[122:125], v[182:185], v[154:157], v[122:125]
	v_mfma_f32_16x16x32_f16 v[110:113], v[198:201], v[134:137], v[110:113]
	v_mfma_f32_16x16x32_f16 v[98:101], v[206:209], v[154:157], v[98:101]
	v_mfma_f32_16x16x32_f16 v[126:129], v[182:185], v[134:137], v[126:129]
	v_mfma_f32_16x16x32_f16 v[122:125], v[186:189], v[168:171], v[122:125]
	v_mfma_f32_16x16x32_f16 v[118:121], v[190:193], v[134:137], v[118:121]
	v_mfma_f32_16x16x32_f16 v[114:117], v[190:193], v[154:157], v[114:117]
	v_mfma_f32_16x16x32_f16 v[130:133], v[202:205], v[138:141], v[110:113]
	v_mfma_f32_16x16x32_f16 v[106:109], v[198:201], v[154:157], v[106:109]
	v_mfma_f32_16x16x32_f16 v[102:105], v[206:209], v[134:137], v[102:105]
	v_mfma_f32_16x16x32_f16 v[98:101], v[210:213], v[168:171], v[98:101]
	v_mfma_f32_16x16x32_f16 v[126:129], v[186:189], v[138:141], v[126:129]
	v_mfma_f32_16x16x32_f16 v[118:121], v[194:197], v[138:141], v[118:121]
	v_mfma_f32_16x16x32_f16 v[114:117], v[194:197], v[168:171], v[114:117]
	v_mfma_f32_16x16x32_f16 v[214:217], v[202:205], v[168:171], v[106:109]
	v_mfma_f32_16x16x32_f16 v[102:105], v[210:213], v[138:141], v[102:105]
	s_barrier
	ds_read_b128 v[106:109], v162
	ds_read_b128 v[110:113], v163
	ds_read_b128 v[160:163], v164
	ds_read_b128 v[218:221], v165
	s_barrier
	s_waitcnt lgkmcnt(0)
	v_mfma_f32_16x16x32_f16 v[82:85], v[190:193], v[160:163], v[82:85]
	v_mfma_f32_16x16x32_f16 v[78:81], v[198:201], v[106:109], v[78:81]
	v_mfma_f32_16x16x32_f16 v[74:77], v[198:201], v[160:163], v[74:77]
	v_mfma_f32_16x16x32_f16 v[70:73], v[206:209], v[106:109], v[70:73]
	v_mfma_f32_16x16x32_f16 v[66:69], v[206:209], v[160:163], v[66:69]
	v_mfma_f32_16x16x32_f16 v[94:97], v[182:185], v[106:109], v[94:97]
	v_mfma_f32_16x16x32_f16 v[90:93], v[182:185], v[160:163], v[90:93]
	v_mfma_f32_16x16x32_f16 v[86:89], v[190:193], v[106:109], v[86:89]
	v_mfma_f32_16x16x32_f16 v[82:85], v[194:197], v[218:221], v[82:85]
	v_mfma_f32_16x16x32_f16 v[78:81], v[202:205], v[110:113], v[78:81]
	v_mfma_f32_16x16x32_f16 v[74:77], v[202:205], v[218:221], v[74:77]
	v_mfma_f32_16x16x32_f16 v[70:73], v[210:213], v[110:113], v[70:73]
	v_mfma_f32_16x16x32_f16 v[66:69], v[210:213], v[218:221], v[66:69]
	v_mfma_f32_16x16x32_f16 v[222:225], v[186:189], v[110:113], v[94:97]
	v_mfma_f32_16x16x32_f16 v[182:185], v[186:189], v[218:221], v[90:93]
	v_mfma_f32_16x16x32_f16 v[86:89], v[194:197], v[110:113], v[86:89]
	s_barrier
	ds_read_b128 v[90:93], v176 offset:16384
	ds_read_b128 v[94:97], v176 offset:17408
	ds_read_b128 v[186:189], v176 offset:18432
	ds_read_b128 v[190:193], v176 offset:19456
	ds_read_b128 v[194:197], v176 offset:20480
	ds_read_b128 v[198:201], v176 offset:21504
	ds_read_b128 v[202:205], v176 offset:22528
	ds_read_b128 v[206:209], v176 offset:23552
	s_waitcnt vmcnt(4)
	s_barrier
	s_waitcnt lgkmcnt(0)
	v_mfma_f32_16x16x32_f16 v[46:49], v[194:197], v[134:137], v[46:49]
	v_mfma_f32_16x16x32_f16 v[42:45], v[194:197], v[154:157], v[42:45]
	v_mfma_f32_16x16x32_f16 v[38:41], v[202:205], v[134:137], v[38:41]
	v_mfma_f32_16x16x32_f16 v[34:37], v[202:205], v[154:157], v[34:37]
	v_mfma_f32_16x16x32_f16 v[62:65], v[90:93], v[134:137], v[62:65]
	v_mfma_f32_16x16x32_f16 v[58:61], v[90:93], v[154:157], v[58:61]
	v_mfma_f32_16x16x32_f16 v[54:57], v[186:189], v[134:137], v[54:57]
	v_mfma_f32_16x16x32_f16 v[50:53], v[186:189], v[154:157], v[50:53]
	v_mfma_f32_16x16x32_f16 v[46:49], v[198:201], v[138:141], v[46:49]
	v_mfma_f32_16x16x32_f16 v[42:45], v[198:201], v[168:171], v[42:45]
	v_mfma_f32_16x16x32_f16 v[38:41], v[206:209], v[138:141], v[38:41]
	v_mfma_f32_16x16x32_f16 v[34:37], v[206:209], v[168:171], v[34:37]
	v_mfma_f32_16x16x32_f16 v[210:213], v[94:97], v[138:141], v[62:65]
	v_mfma_f32_16x16x32_f16 v[226:229], v[94:97], v[168:171], v[58:61]
	v_mfma_f32_16x16x32_f16 v[230:233], v[190:193], v[138:141], v[54:57]
	v_mfma_f32_16x16x32_f16 v[234:237], v[190:193], v[168:171], v[50:53]
	v_mfma_f32_16x16x32_f16 v[2:5], v[202:205], v[160:163], v[2:5]
	v_mfma_f32_16x16x32_f16 v[30:33], v[90:93], v[106:109], v[30:33]
	v_mfma_f32_16x16x32_f16 v[26:29], v[90:93], v[160:163], v[26:29]
	v_mfma_f32_16x16x32_f16 v[22:25], v[186:189], v[106:109], v[22:25]
	v_mfma_f32_16x16x32_f16 v[18:21], v[186:189], v[160:163], v[18:21]
	v_mfma_f32_16x16x32_f16 v[14:17], v[194:197], v[106:109], v[14:17]
	v_mfma_f32_16x16x32_f16 v[10:13], v[194:197], v[160:163], v[10:13]
	v_mfma_f32_16x16x32_f16 v[6:9], v[202:205], v[106:109], v[6:9]
	v_mfma_f32_16x16x32_f16 v[2:5], v[206:209], v[218:221], v[2:5]
	v_mfma_f32_16x16x32_f16 v[138:141], v[94:97], v[110:113], v[30:33]
	v_mfma_f32_16x16x32_f16 v[168:171], v[94:97], v[218:221], v[26:29]
	v_mfma_f32_16x16x32_f16 v[238:241], v[190:193], v[110:113], v[22:25]
	v_mfma_f32_16x16x32_f16 v[186:189], v[190:193], v[218:221], v[18:21]
	v_mfma_f32_16x16x32_f16 v[190:193], v[198:201], v[110:113], v[14:17]
	v_mfma_f32_16x16x32_f16 v[194:197], v[198:201], v[218:221], v[10:13]
	v_mfma_f32_16x16x32_f16 v[198:201], v[206:209], v[110:113], v[6:9]
	s_barrier
	s_nop 0
	ds_read_b128 v[6:9], v144
	ds_read_b128 v[10:13], v145
	ds_read_b128 v[14:17], v146
	ds_read_b128 v[160:163], v147
	ds_read_b128 v[18:21], v176 offset:32768
	ds_read_b128 v[22:25], v176 offset:33792
	ds_read_b128 v[26:29], v176 offset:34816
	ds_read_b128 v[50:53], v176 offset:35840
	ds_read_b128 v[202:205], v176 offset:36864
	ds_read_b128 v[206:209], v176 offset:37888
	ds_read_b128 v[218:221], v176 offset:38912
	ds_read_b128 v[242:245], v176 offset:39936
	s_waitcnt vmcnt(2)
	s_barrier
	s_waitcnt lgkmcnt(0)
	v_mfma_f32_16x16x32_f16 v[30:33], v[18:21], v[6:9], v[126:129]
	v_mfma_f32_16x16x32_f16 v[154:157], v[22:25], v[10:13], v[30:33]
	v_mfma_f32_16x16x32_f16 v[30:33], v[18:21], v[14:17], v[122:125]
	v_mfma_f32_16x16x32_f16 v[110:113], v[22:25], v[160:163], v[30:33]
	v_mfma_f32_16x16x32_f16 v[30:33], v[26:29], v[6:9], v[118:121]
	v_mfma_f32_16x16x32_f16 v[146:149], v[50:53], v[10:13], v[30:33]
	v_mfma_f32_16x16x32_f16 v[30:33], v[26:29], v[14:17], v[114:117]
	v_mfma_f32_16x16x32_f16 v[106:109], v[50:53], v[160:163], v[30:33]
	v_mfma_f32_16x16x32_f16 v[30:33], v[202:205], v[6:9], v[130:133]
	v_mfma_f32_16x16x32_f16 v[142:145], v[206:209], v[10:13], v[30:33]
	v_mfma_f32_16x16x32_f16 v[30:33], v[202:205], v[14:17], v[214:217]
	v_mfma_f32_16x16x32_f16 v[94:97], v[206:209], v[160:163], v[30:33]
	v_mfma_f32_16x16x32_f16 v[30:33], v[218:221], v[6:9], v[102:105]
	v_mfma_f32_16x16x32_f16 v[134:137], v[242:245], v[10:13], v[30:33]
	v_mfma_f32_16x16x32_f16 v[30:33], v[218:221], v[14:17], v[98:101]
	v_mfma_f32_16x16x32_f16 v[90:93], v[242:245], v[160:163], v[30:33]
	s_barrier
	ds_read_b128 v[102:105], v150
	ds_read_b128 v[114:117], v151
	ds_read_b128 v[118:121], v152
	ds_read_b128 v[126:129], v153
	s_waitcnt vmcnt(0)
	s_barrier
	s_waitcnt lgkmcnt(0)
	v_mfma_f32_16x16x32_f16 v[30:33], v[18:21], v[102:105], v[222:225]
	v_mfma_f32_16x16x32_f16 v[18:21], v[18:21], v[118:121], v[182:185]
	v_mfma_f32_16x16x32_f16 v[62:65], v[22:25], v[114:117], v[30:33]
	v_mfma_f32_16x16x32_f16 v[30:33], v[22:25], v[126:129], v[18:21]
	v_mfma_f32_16x16x32_f16 v[18:21], v[26:29], v[102:105], v[86:89]
	v_mfma_f32_16x16x32_f16 v[58:61], v[50:53], v[114:117], v[18:21]
	v_mfma_f32_16x16x32_f16 v[18:21], v[26:29], v[118:121], v[82:85]
	v_mfma_f32_16x16x32_f16 v[26:29], v[50:53], v[126:129], v[18:21]
	v_mfma_f32_16x16x32_f16 v[18:21], v[202:205], v[102:105], v[78:81]
	v_mfma_f32_16x16x32_f16 v[54:57], v[206:209], v[114:117], v[18:21]
	v_mfma_f32_16x16x32_f16 v[18:21], v[202:205], v[118:121], v[74:77]
	v_mfma_f32_16x16x32_f16 v[22:25], v[206:209], v[126:129], v[18:21]
	v_mfma_f32_16x16x32_f16 v[18:21], v[218:221], v[102:105], v[70:73]
	v_mfma_f32_16x16x32_f16 v[50:53], v[242:245], v[114:117], v[18:21]
	v_mfma_f32_16x16x32_f16 v[18:21], v[218:221], v[118:121], v[66:69]
	v_mfma_f32_16x16x32_f16 v[18:21], v[242:245], v[126:129], v[18:21]
	s_barrier
	ds_read_b128 v[86:89], v176 offset:49152
	ds_read_b128 v[150:153], v176 offset:50176
	ds_read_b128 v[182:185], v176 offset:51200
	ds_read_b128 v[202:205], v176 offset:52224
	ds_read_b128 v[206:209], v176 offset:53248
	ds_read_b128 v[214:217], v176 offset:54272
	ds_read_b128 v[218:221], v176 offset:55296
	ds_read_b128 v[174:177], v176 offset:56320
	s_barrier
	s_waitcnt lgkmcnt(0)
	v_mfma_f32_16x16x32_f16 v[66:69], v[86:89], v[6:9], v[210:213]
	v_mfma_f32_16x16x32_f16 v[130:133], v[150:153], v[10:13], v[66:69]
	v_mfma_f32_16x16x32_f16 v[66:69], v[86:89], v[14:17], v[226:229]
	v_mfma_f32_16x16x32_f16 v[78:81], v[150:153], v[160:163], v[66:69]
	v_mfma_f32_16x16x32_f16 v[66:69], v[182:185], v[6:9], v[230:233]
	v_mfma_f32_16x16x32_f16 v[46:49], v[206:209], v[6:9], v[46:49]
	v_mfma_f32_16x16x32_f16 v[6:9], v[218:221], v[6:9], v[38:41]
	v_mfma_f32_16x16x32_f16 v[122:125], v[202:205], v[10:13], v[66:69]
	v_mfma_f32_16x16x32_f16 v[66:69], v[182:185], v[14:17], v[234:237]
	v_mfma_f32_16x16x32_f16 v[42:45], v[206:209], v[14:17], v[42:45]
	v_mfma_f32_16x16x32_f16 v[82:85], v[174:177], v[10:13], v[6:9]
	v_mfma_f32_16x16x32_f16 v[6:9], v[218:221], v[14:17], v[34:37]
	v_mfma_f32_16x16x32_f16 v[74:77], v[202:205], v[160:163], v[66:69]
	v_mfma_f32_16x16x32_f16 v[98:101], v[214:217], v[10:13], v[46:49]
	v_mfma_f32_16x16x32_f16 v[70:73], v[214:217], v[160:163], v[42:45]
	v_mfma_f32_16x16x32_f16 v[66:69], v[174:177], v[160:163], v[6:9]
	v_mfma_f32_16x16x32_f16 v[6:9], v[86:89], v[102:105], v[138:141]
	v_mfma_f32_16x16x32_f16 v[46:49], v[150:153], v[114:117], v[6:9]
	v_mfma_f32_16x16x32_f16 v[6:9], v[86:89], v[118:121], v[168:171]
	v_mfma_f32_16x16x32_f16 v[14:17], v[150:153], v[126:129], v[6:9]
	v_mfma_f32_16x16x32_f16 v[6:9], v[182:185], v[102:105], v[238:241]
	v_mfma_f32_16x16x32_f16 v[42:45], v[202:205], v[114:117], v[6:9]
	v_mfma_f32_16x16x32_f16 v[6:9], v[182:185], v[118:121], v[186:189]
	v_mfma_f32_16x16x32_f16 v[10:13], v[202:205], v[126:129], v[6:9]
	v_mfma_f32_16x16x32_f16 v[6:9], v[206:209], v[102:105], v[190:193]
	v_mfma_f32_16x16x32_f16 v[38:41], v[214:217], v[114:117], v[6:9]
	v_mfma_f32_16x16x32_f16 v[6:9], v[206:209], v[118:121], v[194:197]
	v_mfma_f32_16x16x32_f16 v[34:37], v[218:221], v[102:105], v[198:201]
	v_mfma_f32_16x16x32_f16 v[2:5], v[218:221], v[118:121], v[2:5]
	v_mfma_f32_16x16x32_f16 v[6:9], v[214:217], v[126:129], v[6:9]
	v_mfma_f32_16x16x32_f16 v[34:37], v[174:177], v[114:117], v[34:37]
	v_mfma_f32_16x16x32_f16 v[2:5], v[174:177], v[126:129], v[2:5]
	s_cmpk_gt_u32 s61, 0xff
	s_barrier
	s_cbranch_scc1 .LBB10_15
	s_barrier
